# fp8 GEMM K-loops: four of the six LDS-DMA pieces of the heavy load segments issued inside the following MFMA segment (vmcnt 8->4)
# baseline (speedup 1.0000x reference)
; #define PG8_STAGE(bufoff, gbase, voff) do { _Pragma("unroll") for (int _i = 0; _i < 2; ++_i) \
;         asm volatile("s_mov_b32 m0, %0\n\ts_nop 0\n\tglobal_load_lds_dwordx4 %1, %2" :: "s"(ldsb + (unsigned)(bufoff) + ldsw + _i * 8192u), "v"((voff)[_i]), "s"((const char*)(gbase)) : "m0", "memory"); } while (0)
; #define PG8_WAIT_V(n) asm volatile("s_waitcnt vmcnt(" #n ")" ::: "memory")
; #define PG8_WAIT_L(n) asm volatile("s_waitcnt lgkmcnt(" #n ")" ::: "memory")
; #define PG8_BAR __builtin_amdgcn_s_barrier()
; #define PG8_SCHED __builtin_amdgcn_sched_barrier(0)
; template <class Epi, class Sched, bool F8 = false, bool MID = false, bool GATHER = false>
; __device__ __forceinline__ void gemm_phase(LAS unsigned char* lds, const Gemm g, const Sched& S, const Epi& E) {
;     ...
;         for (int t = 0; t < nt; t += 2) {
;             const bool last = (t == nt - 2);
;             const char* a1 = cA + (size_t)(t + 1) * kstep;
;             const char* a2 = last ? nA : cA + (size_t)(t + 2) * kstep; const char* b2 = last ? nB : cB + (size_t)(t + 2) * kstep;
;             const char* a3 = a2 + kstep; const char* b3 = b2 + kstep;
;             unsigned xA0[2], xA1[2];
; #pragma unroll
;             for (int i = 0; i < 2; ++i) { xA0[i] = last ? nvA0[i] : voffA[i]; xA1[i] = last ? nvA1[i] : voffA1[i]; }
;             if constexpr (MID) { if (t == (nt >> 1)) { if constexpr (F8) asm volatile("s_nop 15\n\ts_nop 15" ::: "memory"); int l_; asm volatile("v_mbcnt_lo_u32_b32 %0, -1, 0\n\tv_mbcnt_hi_u32_b32 %0, -1, %0" : "=v"(l_)); E.mid(acc, cur, wr, wc, l_ & 15, l_ >> 4); if constexpr (F8) asm volatile("s_nop 7" ::: "memory"); } }
;             PG8_LDB(B0, 0, 0); PG8_LDB(B1, 0, 1); PG8_SCHED; PG8_LDA(At, 0, 0); PG8_STAGE(PG8_SA(1, 1), a1, voffA1);
;             PG8_WAIT_V(8); PG8_WAIT_L(0); PG8_BAR; PG8_MMA(0, 0, At, B0); PG8_MMA(0, 1, At, B1); PG8_BAR; PG8_SCHED;
;             PG8_LDA(At, 0, 1); PG8_STAGE(PG8_SB(0, 0), b2, voffB); PG8_STAGE(PG8_SB(0, 1), b2 + hstepB, voffB); PG8_STAGE(PG8_SA(0, 0), a2, xA0);
;             PG8_WAIT_V(8); PG8_WAIT_L(0); PG8_BAR; PG8_MMA(1, 0, At, B0); PG8_MMA(1, 1, At, B1); PG8_BAR; PG8_SCHED;
.LBB0_1161:
	ds_read_b128 v[18:21], v170
	ds_read_b128 v[22:25], v170 offset:1024
	ds_read_b128 v[26:29], v170 offset:2048
	ds_read_b128 v[30:33], v170 offset:3072
	s_waitcnt lgkmcnt(4)
	ds_read_b128 v[2:5], v171
	ds_read_b128 v[6:9], v171 offset:1024
	ds_read_b128 v[10:13], v171 offset:2048
	ds_read_b128 v[14:17], v171 offset:3072
	s_add_u32 s4, s54, 0x100
	s_addc_u32 s5, s55, 0
	s_cmp_eq_u32 s79, 12
	s_cselect_b32 s60, s48, s4
	s_cselect_b32 s61, s49, s5
	s_cselect_b32 s56, s50, vcc_lo
	s_cselect_b32 s57, s51, vcc_hi
	s_add_u32 s58, s60, 0x80
	s_addc_u32 s59, s61, 0
	s_add_u32 s54, s54, 0x80
	s_addc_u32 s55, s55, 0
	ds_read_b128 v[178:181], v172
	ds_read_b128 v[182:185], v172 offset:1024
	ds_read_b128 v[186:189], v172 offset:2048
	ds_read_b128 v[190:193], v172 offset:3072
	ds_read_b128 v[194:197], v172 offset:4096
	ds_read_b128 v[198:201], v172 offset:5120
	ds_read_b128 v[202:205], v172 offset:6144
	ds_read_b128 v[206:209], v172 offset:7168
	s_mov_b32 m0, s89
	s_nop 0
	global_load_lds_dwordx4 v163, s[54:55]
	s_nop 0
	s_mov_b32 m0, s90
	s_nop 0
	global_load_lds_dwordx4 v168, s[54:55]
	s_waitcnt vmcnt(8)
	s_waitcnt lgkmcnt(0)
	s_barrier
	s_setprio 1
	s_waitcnt lgkmcnt(6)
	v_mfma_scale_f32_16x16x128_f8f6f4 v[158:161], v[18:25], v[178:185], v[158:161], v173, v174 op_sel_hi:[0,0,0]
	v_mfma_scale_f32_16x16x128_f8f6f4 v[154:157], v[26:33], v[178:185], v[154:157], v173, v174 op_sel_hi:[0,0,0]
	s_waitcnt lgkmcnt(4)
	v_mfma_scale_f32_16x16x128_f8f6f4 v[142:145], v[18:25], v[186:193], v[142:145], v173, v174 op_sel_hi:[0,0,0]
	v_mfma_scale_f32_16x16x128_f8f6f4 v[138:141], v[26:33], v[186:193], v[138:141], v173, v174 op_sel_hi:[0,0,0]
	s_waitcnt lgkmcnt(2)
	v_mfma_scale_f32_16x16x128_f8f6f4 v[130:133], v[18:25], v[194:201], v[130:133], v173, v174 op_sel_hi:[0,0,0]
	v_mfma_scale_f32_16x16x128_f8f6f4 v[122:125], v[26:33], v[194:201], v[122:125], v173, v174 op_sel_hi:[0,0,0]
	s_waitcnt lgkmcnt(0)
	v_mfma_scale_f32_16x16x128_f8f6f4 v[114:117], v[18:25], v[202:209], v[114:117], v173, v174 op_sel_hi:[0,0,0]
	v_mfma_scale_f32_16x16x128_f8f6f4 v[106:109], v[26:33], v[202:209], v[106:109], v173, v174 op_sel_hi:[0,0,0]
	s_setprio 0
	s_setprio 1
	v_mfma_scale_f32_16x16x128_f8f6f4 v[150:153], v[2:9], v[178:185], v[150:153], v173, v174 op_sel_hi:[0,0,0]
	v_mfma_scale_f32_16x16x128_f8f6f4 v[146:149], v[10:17], v[178:185], v[146:149], v173, v174 op_sel_hi:[0,0,0]
	v_mfma_scale_f32_16x16x128_f8f6f4 v[134:137], v[2:9], v[186:193], v[134:137], v173, v174 op_sel_hi:[0,0,0]
	v_mfma_scale_f32_16x16x128_f8f6f4 v[126:129], v[10:17], v[186:193], v[126:129], v173, v174 op_sel_hi:[0,0,0]
	v_mfma_scale_f32_16x16x128_f8f6f4 v[118:121], v[2:9], v[194:201], v[118:121], v173, v174 op_sel_hi:[0,0,0]
	v_mfma_scale_f32_16x16x128_f8f6f4 v[110:113], v[10:17], v[194:201], v[110:113], v173, v174 op_sel_hi:[0,0,0]
	v_mfma_scale_f32_16x16x128_f8f6f4 v[102:105], v[2:9], v[202:209], v[102:105], v173, v174 op_sel_hi:[0,0,0]
	v_mfma_scale_f32_16x16x128_f8f6f4 v[98:101], v[10:17], v[202:209], v[98:101], v173, v174 op_sel_hi:[0,0,0]
	s_setprio 0
	s_barrier
	ds_read_b128 v[178:181], v172 offset:16384
	ds_read_b128 v[182:185], v172 offset:17408
	ds_read_b128 v[186:189], v172 offset:18432
	ds_read_b128 v[190:193], v172 offset:19456
	ds_read_b128 v[194:197], v172 offset:20480
	ds_read_b128 v[198:201], v172 offset:21504
	ds_read_b128 v[202:205], v172 offset:22528
	ds_read_b128 v[206:209], v172 offset:23552
	s_mov_b32 m0, s26
	s_nop 0
	global_load_lds_dwordx4 v165, s[56:57]
	s_add_u32 s54, s56, 0x40000
	s_mov_b32 m0, s27
	s_nop 0
	global_load_lds_dwordx4 v169, s[56:57]
	s_addc_u32 s55, s57, 0
	s_waitcnt vmcnt(4)
	s_waitcnt lgkmcnt(0)
	s_barrier
	s_setprio 1
	s_waitcnt lgkmcnt(6)
	v_mfma_scale_f32_16x16x128_f8f6f4 v[94:97], v[18:25], v[178:185], v[94:97], v173, v174 op_sel_hi:[0,0,0]
	v_mfma_scale_f32_16x16x128_f8f6f4 v[90:93], v[26:33], v[178:185], v[90:93], v173, v174 op_sel_hi:[0,0,0]
	s_mov_b32 m0, s62
	s_nop 0
	global_load_lds_dwordx4 v165, s[54:55]
	s_waitcnt lgkmcnt(4)
	v_mfma_scale_f32_16x16x128_f8f6f4 v[70:73], v[18:25], v[186:193], v[70:73], v173, v174 op_sel_hi:[0,0,0]
	v_mfma_scale_f32_16x16x128_f8f6f4 v[66:69], v[26:33], v[186:193], v[66:69], v173, v174 op_sel_hi:[0,0,0]
	s_mov_b32 m0, s63
	s_nop 0
	global_load_lds_dwordx4 v169, s[54:55]
	s_waitcnt lgkmcnt(2)
	v_mfma_scale_f32_16x16x128_f8f6f4 v[50:53], v[18:25], v[194:201], v[50:53], v173, v174 op_sel_hi:[0,0,0]
	v_mfma_scale_f32_16x16x128_f8f6f4 v[42:45], v[26:33], v[194:201], v[42:45], v173, v174 op_sel_hi:[0,0,0]
	s_mov_b32 m0, s3
	s_nop 0
	global_load_lds_dwordx4 v162, s[60:61]
	s_waitcnt lgkmcnt(0)
	v_mfma_scale_f32_16x16x128_f8f6f4 v[38:41], v[18:25], v[202:209], v[38:41], v173, v174 op_sel_hi:[0,0,0]
	v_mfma_scale_f32_16x16x128_f8f6f4 v[34:37], v[26:33], v[202:209], v[34:37], v173, v174 op_sel_hi:[0,0,0]
	s_mov_b32 m0, s64
	s_nop 0
	global_load_lds_dwordx4 v167, s[60:61]
	s_setprio 0
	s_setprio 1
	v_mfma_scale_f32_16x16x128_f8f6f4 v[86:89], v[2:9], v[178:185], v[86:89], v173, v174 op_sel_hi:[0,0,0]
	v_mfma_scale_f32_16x16x128_f8f6f4 v[74:77], v[10:17], v[178:185], v[74:77], v173, v174 op_sel_hi:[0,0,0]
	v_mfma_scale_f32_16x16x128_f8f6f4 v[54:57], v[2:9], v[186:193], v[54:57], v173, v174 op_sel_hi:[0,0,0]
	v_mfma_scale_f32_16x16x128_f8f6f4 v[46:49], v[10:17], v[186:193], v[46:49], v173, v174 op_sel_hi:[0,0,0]
	v_mfma_scale_f32_16x16x128_f8f6f4 v[82:85], v[2:9], v[194:201], v[82:85], v173, v174 op_sel_hi:[0,0,0]
	v_mfma_scale_f32_16x16x128_f8f6f4 v[78:81], v[10:17], v[194:201], v[78:81], v173, v174 op_sel_hi:[0,0,0]
	v_mfma_scale_f32_16x16x128_f8f6f4 v[62:65], v[2:9], v[202:209], v[62:65], v173, v174 op_sel_hi:[0,0,0]
	v_mfma_scale_f32_16x16x128_f8f6f4 v[58:61], v[10:17], v[202:209], v[58:61], v173, v174 op_sel_hi:[0,0,0]
	s_setprio 0
	s_barrier
; #define PG8_STAGE(bufoff, gbase, voff) do { _Pragma("unroll") for (int _i = 0; _i < 2; ++_i) \
;         asm volatile("s_mov_b32 m0, %0\n\ts_nop 0\n\tglobal_load_lds_dwordx4 %1, %2" :: "s"(ldsb + (unsigned)(bufoff) + ldsw + _i * 8192u), "v"((voff)[_i]), "s"((const char*)(gbase)) : "m0", "memory"); } while (0)
; #define PG8_WAIT_V(n) asm volatile("s_waitcnt vmcnt(" #n ")" ::: "memory")
; #define PG8_WAIT_L(n) asm volatile("s_waitcnt lgkmcnt(" #n ")" ::: "memory")
; #define PG8_BAR __builtin_amdgcn_s_barrier()
; #define PG8_SCHED __builtin_amdgcn_sched_barrier(0)
; template <class Epi, class Sched, bool F8 = false, bool MID = false, bool GATHER = false>
; __device__ __forceinline__ void gemm_phase(LAS unsigned char* lds, const Gemm g, const Sched& S, const Epi& E) {
;     ...
;             PG8_LDB(B0, 1, 0); PG8_LDB(B1, 1, 1); PG8_SCHED; PG8_LDA(At, 1, 0); PG8_STAGE(PG8_SA(0, 1), a2, xA1);
;             PG8_WAIT_V(8); PG8_WAIT_L(0); PG8_BAR; PG8_MMA(0, 0, At, B0); PG8_MMA(0, 1, At, B1); PG8_BAR; PG8_SCHED;
;             PG8_LDA(At, 1, 1); PG8_STAGE(PG8_SB(1, 0), b3, voffB); PG8_STAGE(PG8_SB(1, 1), b3 + hstepB, voffB); PG8_STAGE(PG8_SA(1, 0), a3, xA0);
;             PG8_WAIT_V(8); PG8_WAIT_L(0); PG8_BAR; PG8_MMA(1, 0, At, B0); PG8_MMA(1, 1, At, B1); PG8_BAR; PG8_SCHED;
;         }
	ds_read_b128 v[2:5], v175
	ds_read_b128 v[6:9], v175 offset:1024
	ds_read_b128 v[10:13], v175 offset:2048
	ds_read_b128 v[14:17], v175 offset:3072
	ds_read_b128 v[18:21], v176
	ds_read_b128 v[22:25], v176 offset:1024
	ds_read_b128 v[26:29], v176 offset:2048
	ds_read_b128 v[30:33], v176 offset:3072
	ds_read_b128 v[178:181], v172 offset:32768
	ds_read_b128 v[182:185], v172 offset:33792
	ds_read_b128 v[186:189], v172 offset:34816
	ds_read_b128 v[190:193], v172 offset:35840
	ds_read_b128 v[194:197], v172 offset:36864
	ds_read_b128 v[198:201], v172 offset:37888
	ds_read_b128 v[202:205], v172 offset:38912
	ds_read_b128 v[206:209], v172 offset:39936
	s_mov_b32 m0, s65
	s_nop 0
	global_load_lds_dwordx4 v163, s[60:61]
	s_nop 0
	s_mov_b32 m0, s66
	s_nop 0
	global_load_lds_dwordx4 v168, s[60:61]
	s_waitcnt vmcnt(8)
	s_waitcnt lgkmcnt(0)
	s_barrier
	s_setprio 1
	s_waitcnt lgkmcnt(6)
	v_mfma_scale_f32_16x16x128_f8f6f4 v[158:161], v[2:9], v[178:185], v[158:161], v173, v174 op_sel_hi:[0,0,0]
	v_mfma_scale_f32_16x16x128_f8f6f4 v[154:157], v[10:17], v[178:185], v[154:157], v173, v174 op_sel_hi:[0,0,0]
	s_waitcnt lgkmcnt(4)
	v_mfma_scale_f32_16x16x128_f8f6f4 v[142:145], v[2:9], v[186:193], v[142:145], v173, v174 op_sel_hi:[0,0,0]
	v_mfma_scale_f32_16x16x128_f8f6f4 v[138:141], v[10:17], v[186:193], v[138:141], v173, v174 op_sel_hi:[0,0,0]
	s_waitcnt lgkmcnt(2)
	v_mfma_scale_f32_16x16x128_f8f6f4 v[130:133], v[2:9], v[194:201], v[130:133], v173, v174 op_sel_hi:[0,0,0]
	v_mfma_scale_f32_16x16x128_f8f6f4 v[122:125], v[10:17], v[194:201], v[122:125], v173, v174 op_sel_hi:[0,0,0]
	s_waitcnt lgkmcnt(0)
	v_mfma_scale_f32_16x16x128_f8f6f4 v[114:117], v[2:9], v[202:209], v[114:117], v173, v174 op_sel_hi:[0,0,0]
	v_mfma_scale_f32_16x16x128_f8f6f4 v[106:109], v[10:17], v[202:209], v[106:109], v173, v174 op_sel_hi:[0,0,0]
	s_setprio 0
	s_setprio 1
	v_mfma_scale_f32_16x16x128_f8f6f4 v[150:153], v[18:25], v[178:185], v[150:153], v173, v174 op_sel_hi:[0,0,0]
	v_mfma_scale_f32_16x16x128_f8f6f4 v[146:149], v[26:33], v[178:185], v[146:149], v173, v174 op_sel_hi:[0,0,0]
	v_mfma_scale_f32_16x16x128_f8f6f4 v[134:137], v[18:25], v[186:193], v[134:137], v173, v174 op_sel_hi:[0,0,0]
	v_mfma_scale_f32_16x16x128_f8f6f4 v[126:129], v[26:33], v[186:193], v[126:129], v173, v174 op_sel_hi:[0,0,0]
	v_mfma_scale_f32_16x16x128_f8f6f4 v[118:121], v[18:25], v[194:201], v[118:121], v173, v174 op_sel_hi:[0,0,0]
	v_mfma_scale_f32_16x16x128_f8f6f4 v[110:113], v[26:33], v[194:201], v[110:113], v173, v174 op_sel_hi:[0,0,0]
	v_mfma_scale_f32_16x16x128_f8f6f4 v[102:105], v[18:25], v[202:209], v[102:105], v173, v174 op_sel_hi:[0,0,0]
	v_mfma_scale_f32_16x16x128_f8f6f4 v[98:101], v[26:33], v[202:209], v[98:101], v173, v174 op_sel_hi:[0,0,0]
	s_setprio 0
	s_barrier
	ds_read_b128 v[178:181], v172 offset:49152
	ds_read_b128 v[182:185], v172 offset:50176
	ds_read_b128 v[186:189], v172 offset:51200
	ds_read_b128 v[190:193], v172 offset:52224
	ds_read_b128 v[194:197], v172 offset:53248
	ds_read_b128 v[198:201], v172 offset:54272
	ds_read_b128 v[202:205], v172 offset:55296
	ds_read_b128 v[206:209], v172 offset:56320
	s_add_u32 s54, s56, 0x80
	s_addc_u32 s55, s57, 0
	s_mov_b32 m0, s70
	s_nop 0
	global_load_lds_dwordx4 v165, s[54:55]
	s_nop 0
	s_mov_b32 m0, s71
	s_nop 0
	global_load_lds_dwordx4 v169, s[54:55]
	s_add_u32 s54, s56, 0x40080
	s_addc_u32 s55, s57, 0
	s_waitcnt vmcnt(4)
	s_waitcnt lgkmcnt(0)
	s_barrier
	s_setprio 1
	s_waitcnt lgkmcnt(6)
	v_mfma_scale_f32_16x16x128_f8f6f4 v[94:97], v[2:9], v[178:185], v[94:97], v173, v174 op_sel_hi:[0,0,0]
	v_mfma_scale_f32_16x16x128_f8f6f4 v[90:93], v[10:17], v[178:185], v[90:93], v173, v174 op_sel_hi:[0,0,0]
	s_mov_b32 m0, s87
	s_nop 0
	global_load_lds_dwordx4 v165, s[54:55]
	s_waitcnt lgkmcnt(4)
	v_mfma_scale_f32_16x16x128_f8f6f4 v[70:73], v[2:9], v[186:193], v[70:73], v173, v174 op_sel_hi:[0,0,0]
	v_mfma_scale_f32_16x16x128_f8f6f4 v[66:69], v[10:17], v[186:193], v[66:69], v173, v174 op_sel_hi:[0,0,0]
	s_mov_b32 m0, s88
	s_nop 0
	global_load_lds_dwordx4 v169, s[54:55]
	s_waitcnt lgkmcnt(2)
	v_mfma_scale_f32_16x16x128_f8f6f4 v[50:53], v[2:9], v[194:201], v[50:53], v173, v174 op_sel_hi:[0,0,0]
	v_mfma_scale_f32_16x16x128_f8f6f4 v[42:45], v[10:17], v[194:201], v[42:45], v173, v174 op_sel_hi:[0,0,0]
	s_mov_b32 m0, s72
	s_nop 0
	global_load_lds_dwordx4 v162, s[58:59]
	s_waitcnt lgkmcnt(0)
	v_mfma_scale_f32_16x16x128_f8f6f4 v[38:41], v[2:9], v[202:209], v[38:41], v173, v174 op_sel_hi:[0,0,0]
	v_mfma_scale_f32_16x16x128_f8f6f4 v[34:37], v[10:17], v[202:209], v[34:37], v173, v174 op_sel_hi:[0,0,0]
	s_mov_b32 m0, s73
	s_nop 0
	global_load_lds_dwordx4 v167, s[58:59]
	s_setprio 0
	s_setprio 1
	v_mfma_scale_f32_16x16x128_f8f6f4 v[86:89], v[18:25], v[178:185], v[86:89], v173, v174 op_sel_hi:[0,0,0]
	v_mfma_scale_f32_16x16x128_f8f6f4 v[74:77], v[26:33], v[178:185], v[74:77], v173, v174 op_sel_hi:[0,0,0]
	v_mfma_scale_f32_16x16x128_f8f6f4 v[54:57], v[18:25], v[186:193], v[54:57], v173, v174 op_sel_hi:[0,0,0]
	v_mfma_scale_f32_16x16x128_f8f6f4 v[46:49], v[26:33], v[186:193], v[46:49], v173, v174 op_sel_hi:[0,0,0]
	v_mfma_scale_f32_16x16x128_f8f6f4 v[82:85], v[18:25], v[194:201], v[82:85], v173, v174 op_sel_hi:[0,0,0]
	v_mfma_scale_f32_16x16x128_f8f6f4 v[78:81], v[26:33], v[194:201], v[78:81], v173, v174 op_sel_hi:[0,0,0]
	v_mfma_scale_f32_16x16x128_f8f6f4 v[62:65], v[18:25], v[202:209], v[62:65], v173, v174 op_sel_hi:[0,0,0]
	v_mfma_scale_f32_16x16x128_f8f6f4 v[58:61], v[26:33], v[202:209], v[58:61], v173, v174 op_sel_hi:[0,0,0]
	s_setprio 0
	s_barrier
	s_add_i32 s79, s79, 2
	s_add_u32 vcc_lo, vcc_lo, 0x100
	s_addc_u32 vcc_hi, vcc_hi, 0
	s_cmp_gt_u32 s79, 13
	s_mov_b64 s[54:55], s[4:5]
	s_cbranch_scc0 .LBB0_1161
	s_and_b64 vcc, exec, s[42:43]
	s_cbranch_vccz .LBB0_1164
	s_barrier

; #define PG8_STAGE(bufoff, gbase, voff) do { _Pragma("unroll") for (int _i = 0; _i < 2; ++_i) \
;         asm volatile("s_mov_b32 m0, %0\n\ts_nop 0\n\tglobal_load_lds_dwordx4 %1, %2" :: "s"(ldsb + (unsigned)(bufoff) + ldsw + _i * 8192u), "v"((voff)[_i]), "s"((const char*)(gbase)) : "m0", "memory"); } while (0)
; #define PG8_WAIT_V(n) asm volatile("s_waitcnt vmcnt(" #n ")" ::: "memory")
; #define PG8_WAIT_L(n) asm volatile("s_waitcnt lgkmcnt(" #n ")" ::: "memory")
; #define PG8_BAR __builtin_amdgcn_s_barrier()
; #define PG8_SCHED __builtin_amdgcn_sched_barrier(0)
; template <class Epi, class Sched, bool F8 = false, bool MID = false, bool GATHER = false>
; __device__ __forceinline__ void gemm_phase(LAS unsigned char* lds, const Gemm g, const Sched& S, const Epi& E) {
;     ...
;         for (int t = 0; t < nt; t += 2) {
;             const bool last = (t == nt - 2);
;             const char* a1 = cA + (size_t)(t + 1) * kstep;
;             const char* a2 = last ? nA : cA + (size_t)(t + 2) * kstep; const char* b2 = last ? nB : cB + (size_t)(t + 2) * kstep;
;             const char* a3 = a2 + kstep; const char* b3 = b2 + kstep;
;             unsigned xA0[2], xA1[2];
; #pragma unroll
;             for (int i = 0; i < 2; ++i) { xA0[i] = last ? nvA0[i] : voffA[i]; xA1[i] = last ? nvA1[i] : voffA1[i]; }
;             if constexpr (MID) { if (t == (nt >> 1)) { if constexpr (F8) asm volatile("s_nop 15\n\ts_nop 15" ::: "memory"); int l_; asm volatile("v_mbcnt_lo_u32_b32 %0, -1, 0\n\tv_mbcnt_hi_u32_b32 %0, -1, %0" : "=v"(l_)); E.mid(acc, cur, wr, wc, l_ & 15, l_ >> 4); if constexpr (F8) asm volatile("s_nop 7" ::: "memory"); } }
;             PG8_LDB(B0, 0, 0); PG8_LDB(B1, 0, 1); PG8_SCHED; PG8_LDA(At, 0, 0); PG8_STAGE(PG8_SA(1, 1), a1, voffA1);
;             PG8_WAIT_V(8); PG8_WAIT_L(0); PG8_BAR; PG8_MMA(0, 0, At, B0); PG8_MMA(0, 1, At, B1); PG8_BAR; PG8_SCHED;
;             PG8_LDA(At, 0, 1); PG8_STAGE(PG8_SB(0, 0), b2, voffB); PG8_STAGE(PG8_SB(0, 1), b2 + hstepB, voffB); PG8_STAGE(PG8_SA(0, 0), a2, xA0);
;             PG8_WAIT_V(8); PG8_WAIT_L(0); PG8_BAR; PG8_MMA(1, 0, At, B0); PG8_MMA(1, 1, At, B1); PG8_BAR; PG8_SCHED;
.LBB0_1931:
	ds_read_b128 v[18:21], v169
	ds_read_b128 v[22:25], v169 offset:1024
	ds_read_b128 v[26:29], v169 offset:2048
	ds_read_b128 v[30:33], v169 offset:3072
	ds_read_b128 v[2:5], v170
	ds_read_b128 v[6:9], v170 offset:1024
	ds_read_b128 v[10:13], v170 offset:2048
	ds_read_b128 v[14:17], v170 offset:3072
	s_add_u32 s52, s54, 0x100
	s_addc_u32 s53, s55, 0
	s_cmp_eq_u32 s96, 12
	s_cselect_b32 s60, s48, s52
	s_cselect_b32 s61, s49, s53
	s_cselect_b32 s56, s50, s94
	s_cselect_b32 s57, s51, s95
	s_add_u32 s58, s60, 0x80
	s_addc_u32 s59, s61, 0
	s_add_u32 s54, s54, 0x80
	s_addc_u32 s55, s55, 0
	ds_read_b128 v[176:179], v171
	ds_read_b128 v[180:183], v171 offset:1024
	ds_read_b128 v[184:187], v171 offset:2048
	ds_read_b128 v[188:191], v171 offset:3072
	ds_read_b128 v[192:195], v171 offset:4096
	ds_read_b128 v[196:199], v171 offset:5120
	ds_read_b128 v[200:203], v171 offset:6144
	ds_read_b128 v[204:207], v171 offset:7168
	s_mov_b32 m0, s77
	s_nop 0
	global_load_lds_dwordx4 v162, s[54:55]
	s_nop 0
	s_mov_b32 m0, s78
	s_nop 0
	global_load_lds_dwordx4 v167, s[54:55]
	s_waitcnt vmcnt(8)
	s_waitcnt lgkmcnt(0)
	s_barrier
	s_setprio 1
	s_waitcnt lgkmcnt(6)
	v_mfma_scale_f32_16x16x128_f8f6f4 v[158:161], v[18:25], v[176:183], v[158:161], v172, v173 op_sel_hi:[0,0,0]
	v_mfma_scale_f32_16x16x128_f8f6f4 v[154:157], v[26:33], v[176:183], v[154:157], v172, v173 op_sel_hi:[0,0,0]
	s_waitcnt lgkmcnt(4)
	v_mfma_scale_f32_16x16x128_f8f6f4 v[150:153], v[18:25], v[184:191], v[150:153], v172, v173 op_sel_hi:[0,0,0]
	v_mfma_scale_f32_16x16x128_f8f6f4 v[142:145], v[26:33], v[184:191], v[142:145], v172, v173 op_sel_hi:[0,0,0]
	s_waitcnt lgkmcnt(2)
	v_mfma_scale_f32_16x16x128_f8f6f4 v[134:137], v[18:25], v[192:199], v[134:137], v172, v173 op_sel_hi:[0,0,0]
	v_mfma_scale_f32_16x16x128_f8f6f4 v[126:129], v[26:33], v[192:199], v[126:129], v172, v173 op_sel_hi:[0,0,0]
	s_waitcnt lgkmcnt(0)
	v_mfma_scale_f32_16x16x128_f8f6f4 v[118:121], v[18:25], v[200:207], v[118:121], v172, v173 op_sel_hi:[0,0,0]
	v_mfma_scale_f32_16x16x128_f8f6f4 v[110:113], v[26:33], v[200:207], v[110:113], v172, v173 op_sel_hi:[0,0,0]
	s_setprio 0
	s_setprio 1
	v_mfma_scale_f32_16x16x128_f8f6f4 v[146:149], v[2:9], v[176:183], v[146:149], v172, v173 op_sel_hi:[0,0,0]
	v_mfma_scale_f32_16x16x128_f8f6f4 v[138:141], v[10:17], v[176:183], v[138:141], v172, v173 op_sel_hi:[0,0,0]
	v_mfma_scale_f32_16x16x128_f8f6f4 v[130:133], v[2:9], v[184:191], v[130:133], v172, v173 op_sel_hi:[0,0,0]
	v_mfma_scale_f32_16x16x128_f8f6f4 v[122:125], v[10:17], v[184:191], v[122:125], v172, v173 op_sel_hi:[0,0,0]
	v_mfma_scale_f32_16x16x128_f8f6f4 v[114:117], v[2:9], v[192:199], v[114:117], v172, v173 op_sel_hi:[0,0,0]
	v_mfma_scale_f32_16x16x128_f8f6f4 v[106:109], v[10:17], v[192:199], v[106:109], v172, v173 op_sel_hi:[0,0,0]
	v_mfma_scale_f32_16x16x128_f8f6f4 v[102:105], v[2:9], v[200:207], v[102:105], v172, v173 op_sel_hi:[0,0,0]
	v_mfma_scale_f32_16x16x128_f8f6f4 v[98:101], v[10:17], v[200:207], v[98:101], v172, v173 op_sel_hi:[0,0,0]
	s_setprio 0
	s_barrier
	ds_read_b128 v[176:179], v171 offset:16384
	ds_read_b128 v[180:183], v171 offset:17408
	ds_read_b128 v[184:187], v171 offset:18432
	ds_read_b128 v[188:191], v171 offset:19456
	ds_read_b128 v[192:195], v171 offset:20480
	ds_read_b128 v[196:199], v171 offset:21504
	ds_read_b128 v[200:203], v171 offset:22528
	ds_read_b128 v[204:207], v171 offset:23552
	s_mov_b32 m0, s27
	s_nop 0
	global_load_lds_dwordx4 v163, s[56:57]
	s_add_u32 s54, s56, 0x40000
	s_mov_b32 m0, s62
	s_nop 0
	global_load_lds_dwordx4 v168, s[56:57]
	s_addc_u32 s55, s57, 0
	s_waitcnt vmcnt(4)
	s_waitcnt lgkmcnt(0)
	s_barrier
	s_setprio 1
	s_waitcnt lgkmcnt(6)
	v_mfma_scale_f32_16x16x128_f8f6f4 v[94:97], v[18:25], v[176:183], v[94:97], v172, v173 op_sel_hi:[0,0,0]
	v_mfma_scale_f32_16x16x128_f8f6f4 v[90:93], v[26:33], v[176:183], v[90:93], v172, v173 op_sel_hi:[0,0,0]
	s_mov_b32 m0, s63
	s_nop 0
	global_load_lds_dwordx4 v163, s[54:55]
	s_waitcnt lgkmcnt(4)
	v_mfma_scale_f32_16x16x128_f8f6f4 v[78:81], v[18:25], v[184:191], v[78:81], v172, v173 op_sel_hi:[0,0,0]
	v_mfma_scale_f32_16x16x128_f8f6f4 v[70:73], v[26:33], v[184:191], v[70:73], v172, v173 op_sel_hi:[0,0,0]
	s_mov_b32 m0, s64
	s_nop 0
	global_load_lds_dwordx4 v168, s[54:55]
	s_waitcnt lgkmcnt(2)
	v_mfma_scale_f32_16x16x128_f8f6f4 v[54:57], v[18:25], v[192:199], v[54:57], v172, v173 op_sel_hi:[0,0,0]
	v_mfma_scale_f32_16x16x128_f8f6f4 v[46:49], v[26:33], v[192:199], v[46:49], v172, v173 op_sel_hi:[0,0,0]
	s_mov_b32 m0, s26
	s_nop 0
	global_load_lds_dwordx4 v1, s[60:61]
	s_waitcnt lgkmcnt(0)
	v_mfma_scale_f32_16x16x128_f8f6f4 v[38:41], v[18:25], v[200:207], v[38:41], v172, v173 op_sel_hi:[0,0,0]
	v_mfma_scale_f32_16x16x128_f8f6f4 v[34:37], v[26:33], v[200:207], v[34:37], v172, v173 op_sel_hi:[0,0,0]
	s_mov_b32 m0, s65
	s_nop 0
	global_load_lds_dwordx4 v165, s[60:61]
	s_setprio 0
	s_setprio 1
	v_mfma_scale_f32_16x16x128_f8f6f4 v[74:77], v[2:9], v[176:183], v[74:77], v172, v173 op_sel_hi:[0,0,0]
	v_mfma_scale_f32_16x16x128_f8f6f4 v[62:65], v[10:17], v[176:183], v[62:65], v172, v173 op_sel_hi:[0,0,0]
	v_mfma_scale_f32_16x16x128_f8f6f4 v[50:53], v[2:9], v[184:191], v[50:53], v172, v173 op_sel_hi:[0,0,0]
	v_mfma_scale_f32_16x16x128_f8f6f4 v[42:45], v[10:17], v[184:191], v[42:45], v172, v173 op_sel_hi:[0,0,0]
	v_mfma_scale_f32_16x16x128_f8f6f4 v[86:89], v[2:9], v[192:199], v[86:89], v172, v173 op_sel_hi:[0,0,0]
	v_mfma_scale_f32_16x16x128_f8f6f4 v[82:85], v[10:17], v[192:199], v[82:85], v172, v173 op_sel_hi:[0,0,0]
	v_mfma_scale_f32_16x16x128_f8f6f4 v[66:69], v[2:9], v[200:207], v[66:69], v172, v173 op_sel_hi:[0,0,0]
	v_mfma_scale_f32_16x16x128_f8f6f4 v[58:61], v[10:17], v[200:207], v[58:61], v172, v173 op_sel_hi:[0,0,0]
	s_setprio 0
	s_barrier
; #define PG8_STAGE(bufoff, gbase, voff) do { _Pragma("unroll") for (int _i = 0; _i < 2; ++_i) \
;         asm volatile("s_mov_b32 m0, %0\n\ts_nop 0\n\tglobal_load_lds_dwordx4 %1, %2" :: "s"(ldsb + (unsigned)(bufoff) + ldsw + _i * 8192u), "v"((voff)[_i]), "s"((const char*)(gbase)) : "m0", "memory"); } while (0)
; #define PG8_WAIT_V(n) asm volatile("s_waitcnt vmcnt(" #n ")" ::: "memory")
; #define PG8_WAIT_L(n) asm volatile("s_waitcnt lgkmcnt(" #n ")" ::: "memory")
; #define PG8_BAR __builtin_amdgcn_s_barrier()
; #define PG8_SCHED __builtin_amdgcn_sched_barrier(0)
; template <class Epi, class Sched, bool F8 = false, bool MID = false, bool GATHER = false>
; __device__ __forceinline__ void gemm_phase(LAS unsigned char* lds, const Gemm g, const Sched& S, const Epi& E) {
;     ...
;             PG8_LDB(B0, 1, 0); PG8_LDB(B1, 1, 1); PG8_SCHED; PG8_LDA(At, 1, 0); PG8_STAGE(PG8_SA(0, 1), a2, xA1);
;             PG8_WAIT_V(8); PG8_WAIT_L(0); PG8_BAR; PG8_MMA(0, 0, At, B0); PG8_MMA(0, 1, At, B1); PG8_BAR; PG8_SCHED;
;             PG8_LDA(At, 1, 1); PG8_STAGE(PG8_SB(1, 0), b3, voffB); PG8_STAGE(PG8_SB(1, 1), b3 + hstepB, voffB); PG8_STAGE(PG8_SA(1, 0), a3, xA0);
;             PG8_WAIT_V(8); PG8_WAIT_L(0); PG8_BAR; PG8_MMA(1, 0, At, B0); PG8_MMA(1, 1, At, B1); PG8_BAR; PG8_SCHED;
;         }
	ds_read_b128 v[2:5], v174
	ds_read_b128 v[6:9], v174 offset:1024
	ds_read_b128 v[10:13], v174 offset:2048
	ds_read_b128 v[14:17], v174 offset:3072
	ds_read_b128 v[18:21], v175
	ds_read_b128 v[22:25], v175 offset:1024
	ds_read_b128 v[26:29], v175 offset:2048
	ds_read_b128 v[30:33], v175 offset:3072
	ds_read_b128 v[176:179], v171 offset:32768
	ds_read_b128 v[180:183], v171 offset:33792
	ds_read_b128 v[184:187], v171 offset:34816
	ds_read_b128 v[188:191], v171 offset:35840
	ds_read_b128 v[192:195], v171 offset:36864
	ds_read_b128 v[196:199], v171 offset:37888
	ds_read_b128 v[200:203], v171 offset:38912
	ds_read_b128 v[204:207], v171 offset:39936
	s_mov_b32 m0, s66
	s_nop 0
	global_load_lds_dwordx4 v162, s[60:61]
	s_nop 0
	s_mov_b32 m0, s67
	s_nop 0
	global_load_lds_dwordx4 v167, s[60:61]
	s_waitcnt vmcnt(8)
	s_waitcnt lgkmcnt(0)
	s_barrier
	s_setprio 1
	s_waitcnt lgkmcnt(6)
	v_mfma_scale_f32_16x16x128_f8f6f4 v[158:161], v[2:9], v[176:183], v[158:161], v172, v173 op_sel_hi:[0,0,0]
	v_mfma_scale_f32_16x16x128_f8f6f4 v[154:157], v[10:17], v[176:183], v[154:157], v172, v173 op_sel_hi:[0,0,0]
	s_waitcnt lgkmcnt(4)
	v_mfma_scale_f32_16x16x128_f8f6f4 v[150:153], v[2:9], v[184:191], v[150:153], v172, v173 op_sel_hi:[0,0,0]
	v_mfma_scale_f32_16x16x128_f8f6f4 v[142:145], v[10:17], v[184:191], v[142:145], v172, v173 op_sel_hi:[0,0,0]
	s_waitcnt lgkmcnt(2)
	v_mfma_scale_f32_16x16x128_f8f6f4 v[134:137], v[2:9], v[192:199], v[134:137], v172, v173 op_sel_hi:[0,0,0]
	v_mfma_scale_f32_16x16x128_f8f6f4 v[126:129], v[10:17], v[192:199], v[126:129], v172, v173 op_sel_hi:[0,0,0]
	s_waitcnt lgkmcnt(0)
	v_mfma_scale_f32_16x16x128_f8f6f4 v[118:121], v[2:9], v[200:207], v[118:121], v172, v173 op_sel_hi:[0,0,0]
	v_mfma_scale_f32_16x16x128_f8f6f4 v[110:113], v[10:17], v[200:207], v[110:113], v172, v173 op_sel_hi:[0,0,0]
	s_setprio 0
	s_setprio 1
	v_mfma_scale_f32_16x16x128_f8f6f4 v[146:149], v[18:25], v[176:183], v[146:149], v172, v173 op_sel_hi:[0,0,0]
	v_mfma_scale_f32_16x16x128_f8f6f4 v[138:141], v[26:33], v[176:183], v[138:141], v172, v173 op_sel_hi:[0,0,0]
	v_mfma_scale_f32_16x16x128_f8f6f4 v[130:133], v[18:25], v[184:191], v[130:133], v172, v173 op_sel_hi:[0,0,0]
	v_mfma_scale_f32_16x16x128_f8f6f4 v[122:125], v[26:33], v[184:191], v[122:125], v172, v173 op_sel_hi:[0,0,0]
	v_mfma_scale_f32_16x16x128_f8f6f4 v[114:117], v[18:25], v[192:199], v[114:117], v172, v173 op_sel_hi:[0,0,0]
	v_mfma_scale_f32_16x16x128_f8f6f4 v[106:109], v[26:33], v[192:199], v[106:109], v172, v173 op_sel_hi:[0,0,0]
	v_mfma_scale_f32_16x16x128_f8f6f4 v[102:105], v[18:25], v[200:207], v[102:105], v172, v173 op_sel_hi:[0,0,0]
	v_mfma_scale_f32_16x16x128_f8f6f4 v[98:101], v[26:33], v[200:207], v[98:101], v172, v173 op_sel_hi:[0,0,0]
	s_setprio 0
	s_barrier
	ds_read_b128 v[176:179], v171 offset:49152
	ds_read_b128 v[180:183], v171 offset:50176
	ds_read_b128 v[184:187], v171 offset:51200
	ds_read_b128 v[188:191], v171 offset:52224
	ds_read_b128 v[192:195], v171 offset:53248
	ds_read_b128 v[196:199], v171 offset:54272
	ds_read_b128 v[200:203], v171 offset:55296
	ds_read_b128 v[204:207], v171 offset:56320
	s_add_u32 s54, s56, 0x80
	s_addc_u32 s55, s57, 0
	s_mov_b32 m0, s70
	s_nop 0
	global_load_lds_dwordx4 v163, s[54:55]
	s_nop 0
	s_mov_b32 m0, s71
	s_nop 0
	global_load_lds_dwordx4 v168, s[54:55]
	s_add_u32 s54, s56, 0x40080
	s_addc_u32 s55, s57, 0
	s_waitcnt vmcnt(4)
	s_waitcnt lgkmcnt(0)
	s_barrier
	s_setprio 1
	s_waitcnt lgkmcnt(6)
	v_mfma_scale_f32_16x16x128_f8f6f4 v[94:97], v[2:9], v[176:183], v[94:97], v172, v173 op_sel_hi:[0,0,0]
	v_mfma_scale_f32_16x16x128_f8f6f4 v[90:93], v[10:17], v[176:183], v[90:93], v172, v173 op_sel_hi:[0,0,0]
	s_mov_b32 m0, s75
	s_nop 0
	global_load_lds_dwordx4 v163, s[54:55]
	s_waitcnt lgkmcnt(4)
	v_mfma_scale_f32_16x16x128_f8f6f4 v[78:81], v[2:9], v[184:191], v[78:81], v172, v173 op_sel_hi:[0,0,0]
	v_mfma_scale_f32_16x16x128_f8f6f4 v[70:73], v[10:17], v[184:191], v[70:73], v172, v173 op_sel_hi:[0,0,0]
	s_mov_b32 m0, s76
	s_nop 0
	global_load_lds_dwordx4 v168, s[54:55]
	s_waitcnt lgkmcnt(2)
	v_mfma_scale_f32_16x16x128_f8f6f4 v[54:57], v[2:9], v[192:199], v[54:57], v172, v173 op_sel_hi:[0,0,0]
	v_mfma_scale_f32_16x16x128_f8f6f4 v[46:49], v[10:17], v[192:199], v[46:49], v172, v173 op_sel_hi:[0,0,0]
	s_mov_b32 m0, s72
	s_nop 0
	global_load_lds_dwordx4 v1, s[58:59]
	s_waitcnt lgkmcnt(0)
	v_mfma_scale_f32_16x16x128_f8f6f4 v[38:41], v[2:9], v[200:207], v[38:41], v172, v173 op_sel_hi:[0,0,0]
	v_mfma_scale_f32_16x16x128_f8f6f4 v[34:37], v[10:17], v[200:207], v[34:37], v172, v173 op_sel_hi:[0,0,0]
	s_mov_b32 m0, s73
	s_nop 0
	global_load_lds_dwordx4 v165, s[58:59]
	s_setprio 0
	s_setprio 1
	v_mfma_scale_f32_16x16x128_f8f6f4 v[74:77], v[18:25], v[176:183], v[74:77], v172, v173 op_sel_hi:[0,0,0]
	v_mfma_scale_f32_16x16x128_f8f6f4 v[62:65], v[26:33], v[176:183], v[62:65], v172, v173 op_sel_hi:[0,0,0]
	v_mfma_scale_f32_16x16x128_f8f6f4 v[50:53], v[18:25], v[184:191], v[50:53], v172, v173 op_sel_hi:[0,0,0]
	v_mfma_scale_f32_16x16x128_f8f6f4 v[42:45], v[26:33], v[184:191], v[42:45], v172, v173 op_sel_hi:[0,0,0]
	v_mfma_scale_f32_16x16x128_f8f6f4 v[86:89], v[18:25], v[192:199], v[86:89], v172, v173 op_sel_hi:[0,0,0]
	v_mfma_scale_f32_16x16x128_f8f6f4 v[82:85], v[26:33], v[192:199], v[82:85], v172, v173 op_sel_hi:[0,0,0]
	v_mfma_scale_f32_16x16x128_f8f6f4 v[66:69], v[18:25], v[200:207], v[66:69], v172, v173 op_sel_hi:[0,0,0]
	v_mfma_scale_f32_16x16x128_f8f6f4 v[58:61], v[26:33], v[200:207], v[58:61], v172, v173 op_sel_hi:[0,0,0]
	s_setprio 0
	s_barrier
	s_add_i32 s96, s96, 2
	s_add_u32 s94, s94, 0x100
	s_addc_u32 s95, s95, 0
	s_cmp_gt_u32 s96, 13
	s_mov_b64 s[54:55], s[52:53]
	s_cbranch_scc0 .LBB0_1931
	s_and_b64 vcc, exec, s[10:11]
	s_cbranch_vccz .LBB0_1934
	s_barrier

; #define PG8_STAGE(bufoff, gbase, voff) do { _Pragma("unroll") for (int _i = 0; _i < 2; ++_i) \
;         asm volatile("s_mov_b32 m0, %0\n\ts_nop 0\n\tglobal_load_lds_dwordx4 %1, %2" :: "s"(ldsb + (unsigned)(bufoff) + ldsw + _i * 8192u), "v"((voff)[_i]), "s"((const char*)(gbase)) : "m0", "memory"); } while (0)
; #define PG8_WAIT_V(n) asm volatile("s_waitcnt vmcnt(" #n ")" ::: "memory")
; #define PG8_WAIT_L(n) asm volatile("s_waitcnt lgkmcnt(" #n ")" ::: "memory")
; #define PG8_BAR __builtin_amdgcn_s_barrier()
; #define PG8_SCHED __builtin_amdgcn_sched_barrier(0)
; template <class Epi, class Sched, bool F8 = false, bool MID = false, bool GATHER = false>
; __device__ __forceinline__ void gemm_phase(LAS unsigned char* lds, const Gemm g, const Sched& S, const Epi& E) {
;     ...
;             for (int i = 0; i < 2; ++i) { nvA0[i] = has_next ? (unsigned)(rt[(ui + 1) * 256 + RA[i]] * g.lda + CA[i]) : voffA[i]; nvA1[i] = has_next ? (unsigned)(rt[(ui + 1) * 256 + HALF + RA[i]] * g.lda + CA[i]) : voffA1[i]; } }
;         for (int t = 0; t < nt; t += 2) {
;             const bool last = (t == nt - 2);
;             const char* a1 = cA + (size_t)(t + 1) * kstep;
;             const char* a2 = last ? nA : cA + (size_t)(t + 2) * kstep; const char* b2 = last ? nB : cB + (size_t)(t + 2) * kstep;
;             const char* a3 = a2 + kstep; const char* b3 = b2 + kstep;
;             unsigned xA0[2], xA1[2];
; #pragma unroll
;             for (int i = 0; i < 2; ++i) { xA0[i] = last ? nvA0[i] : voffA[i]; xA1[i] = last ? nvA1[i] : voffA1[i]; }
;             if constexpr (MID) { if (t == (nt >> 1)) { if constexpr (F8) asm volatile("s_nop 15\n\ts_nop 15" ::: "memory"); int l_; asm volatile("v_mbcnt_lo_u32_b32 %0, -1, 0\n\tv_mbcnt_hi_u32_b32 %0, -1, %0" : "=v"(l_)); E.mid(acc, cur, wr, wc, l_ & 15, l_ >> 4); if constexpr (F8) asm volatile("s_nop 7" ::: "memory"); } }
;             PG8_LDB(B0, 0, 0); PG8_LDB(B1, 0, 1); PG8_SCHED; PG8_LDA(At, 0, 0); PG8_STAGE(PG8_SA(1, 1), a1, voffA1);
;             PG8_WAIT_V(8); PG8_WAIT_L(0); PG8_BAR; PG8_MMA(0, 0, At, B0); PG8_MMA(0, 1, At, B1); PG8_BAR; PG8_SCHED;
;             PG8_LDA(At, 0, 1); PG8_STAGE(PG8_SB(0, 0), b2, voffB); PG8_STAGE(PG8_SB(0, 1), b2 + hstepB, voffB); PG8_STAGE(PG8_SA(0, 0), a2, xA0);
;             PG8_WAIT_V(8); PG8_WAIT_L(0); PG8_BAR; PG8_MMA(1, 0, At, B0); PG8_MMA(1, 1, At, B1); PG8_BAR; PG8_SCHED;
.LBB0_2474:
	s_add_u32 s22, s34, s64
	s_addc_u32 s23, s35, s65
	s_add_u32 s57, s22, 0x100
	s_addc_u32 s68, s23, 0
	s_add_u32 s66, s16, s64
	s_addc_u32 s67, s17, s65
	s_add_u32 s69, s66, 0x100
	s_addc_u32 s83, s67, 0
	v_add_u32_e32 v2, 0x10000, v172
	v_add_u32_e32 v14, 0x14000, v172
	s_cmp_eq_u32 s13, 12
	ds_read_b128 v[18:21], v2
	ds_read_b128 v[22:25], v2 offset:1024
	ds_read_b128 v[26:29], v2 offset:2048
	ds_read_b128 v[30:33], v2 offset:3072
	ds_read_b128 v[2:5], v14
	ds_read_b128 v[6:9], v14 offset:1024
	ds_read_b128 v[10:13], v14 offset:2048
	ds_read_b128 v[14:17], v14 offset:3072
	s_cselect_b64 vcc, -1, 0
	s_and_b64 s[66:67], vcc, exec
	s_cselect_b32 s70, s62, s57
	s_cselect_b32 s71, s63, s68
	s_cselect_b32 s66, s60, s69
	s_cselect_b32 s67, s61, s83
	s_add_u32 s68, s70, 0x80
	s_addc_u32 s69, s71, 0
	s_add_u32 s22, s22, 0x80
	v_cndmask_b32_e32 v181, v169, v177, vcc
	v_cndmask_b32_e32 v183, v168, v178, vcc
	v_cndmask_b32_e32 v182, v171, v179, vcc
	v_cndmask_b32_e32 v216, v170, v180, vcc
	s_addc_u32 s23, s23, 0
	ds_read_b128 v[184:187], v173
	ds_read_b128 v[188:191], v173 offset:1024
	ds_read_b128 v[192:195], v173 offset:2048
	ds_read_b128 v[196:199], v173 offset:3072
	ds_read_b128 v[200:203], v173 offset:4096
	ds_read_b128 v[204:207], v173 offset:5120
	ds_read_b128 v[208:211], v173 offset:6144
	ds_read_b128 v[212:215], v173 offset:7168
	s_mov_b32 m0, s95
	s_nop 0
	global_load_lds_dwordx4 v168, s[22:23]
	s_nop 0
	s_mov_b32 m0, s96
	s_nop 0
	global_load_lds_dwordx4 v170, s[22:23]
	s_waitcnt vmcnt(8)
	s_waitcnt lgkmcnt(0)
	s_barrier
	s_setprio 1
	s_waitcnt lgkmcnt(6)
	v_mfma_scale_f32_16x16x128_f8f6f4 v[158:161], v[18:25], v[184:191], v[158:161], v174, v175 op_sel_hi:[0,0,0]
	v_mfma_scale_f32_16x16x128_f8f6f4 v[154:157], v[26:33], v[184:191], v[154:157], v174, v175 op_sel_hi:[0,0,0]
	s_waitcnt lgkmcnt(4)
	v_mfma_scale_f32_16x16x128_f8f6f4 v[150:153], v[18:25], v[192:199], v[150:153], v174, v175 op_sel_hi:[0,0,0]
	v_mfma_scale_f32_16x16x128_f8f6f4 v[146:149], v[26:33], v[192:199], v[146:149], v174, v175 op_sel_hi:[0,0,0]
	s_waitcnt lgkmcnt(2)
	v_mfma_scale_f32_16x16x128_f8f6f4 v[142:145], v[18:25], v[200:207], v[142:145], v174, v175 op_sel_hi:[0,0,0]
	v_mfma_scale_f32_16x16x128_f8f6f4 v[138:141], v[26:33], v[200:207], v[138:141], v174, v175 op_sel_hi:[0,0,0]
	s_waitcnt lgkmcnt(0)
	v_mfma_scale_f32_16x16x128_f8f6f4 v[134:137], v[18:25], v[208:215], v[134:137], v174, v175 op_sel_hi:[0,0,0]
	v_mfma_scale_f32_16x16x128_f8f6f4 v[130:133], v[26:33], v[208:215], v[130:133], v174, v175 op_sel_hi:[0,0,0]
	s_setprio 0
	s_setprio 1
	v_mfma_scale_f32_16x16x128_f8f6f4 v[126:129], v[2:9], v[184:191], v[126:129], v174, v175 op_sel_hi:[0,0,0]
	v_mfma_scale_f32_16x16x128_f8f6f4 v[122:125], v[10:17], v[184:191], v[122:125], v174, v175 op_sel_hi:[0,0,0]
	v_mfma_scale_f32_16x16x128_f8f6f4 v[118:121], v[2:9], v[192:199], v[118:121], v174, v175 op_sel_hi:[0,0,0]
	v_mfma_scale_f32_16x16x128_f8f6f4 v[114:117], v[10:17], v[192:199], v[114:117], v174, v175 op_sel_hi:[0,0,0]
	v_mfma_scale_f32_16x16x128_f8f6f4 v[110:113], v[2:9], v[200:207], v[110:113], v174, v175 op_sel_hi:[0,0,0]
	v_mfma_scale_f32_16x16x128_f8f6f4 v[106:109], v[10:17], v[200:207], v[106:109], v174, v175 op_sel_hi:[0,0,0]
	v_mfma_scale_f32_16x16x128_f8f6f4 v[102:105], v[2:9], v[208:215], v[102:105], v174, v175 op_sel_hi:[0,0,0]
	v_mfma_scale_f32_16x16x128_f8f6f4 v[98:101], v[10:17], v[208:215], v[98:101], v174, v175 op_sel_hi:[0,0,0]
	s_setprio 0
	s_barrier
	ds_read_b128 v[184:187], v173 offset:16384
	ds_read_b128 v[188:191], v173 offset:17408
	ds_read_b128 v[192:195], v173 offset:18432
	ds_read_b128 v[196:199], v173 offset:19456
	ds_read_b128 v[200:203], v173 offset:20480
	ds_read_b128 v[204:207], v173 offset:21504
	ds_read_b128 v[208:211], v173 offset:22528
	ds_read_b128 v[212:215], v173 offset:23552
	s_mov_b32 m0, s74
	s_nop 0
	global_load_lds_dwordx4 v163, s[66:67]
	s_add_u32 s22, s66, 0x40000
	s_mov_b32 m0, s75
	s_nop 0
	global_load_lds_dwordx4 v167, s[66:67]
	s_addc_u32 s23, s67, 0
	s_waitcnt vmcnt(4)
	s_waitcnt lgkmcnt(0)
	s_barrier
	s_setprio 1
	s_waitcnt lgkmcnt(6)
	v_mfma_scale_f32_16x16x128_f8f6f4 v[94:97], v[18:25], v[184:191], v[94:97], v174, v175 op_sel_hi:[0,0,0]
	v_mfma_scale_f32_16x16x128_f8f6f4 v[90:93], v[26:33], v[184:191], v[90:93], v174, v175 op_sel_hi:[0,0,0]
	s_mov_b32 m0, s76
	s_nop 0
	global_load_lds_dwordx4 v163, s[22:23]
	s_waitcnt lgkmcnt(4)
	v_mfma_scale_f32_16x16x128_f8f6f4 v[86:89], v[18:25], v[192:199], v[86:89], v174, v175 op_sel_hi:[0,0,0]
	v_mfma_scale_f32_16x16x128_f8f6f4 v[82:85], v[26:33], v[192:199], v[82:85], v174, v175 op_sel_hi:[0,0,0]
	s_mov_b32 m0, s78
	s_nop 0
	global_load_lds_dwordx4 v167, s[22:23]
	s_waitcnt lgkmcnt(2)
	v_mfma_scale_f32_16x16x128_f8f6f4 v[78:81], v[18:25], v[200:207], v[78:81], v174, v175 op_sel_hi:[0,0,0]
	v_mfma_scale_f32_16x16x128_f8f6f4 v[74:77], v[26:33], v[200:207], v[74:77], v174, v175 op_sel_hi:[0,0,0]
	s_mov_b32 m0, s73
	s_nop 0
	global_load_lds_dwordx4 v181, s[70:71]
	s_waitcnt lgkmcnt(0)
	v_mfma_scale_f32_16x16x128_f8f6f4 v[70:73], v[18:25], v[208:215], v[70:73], v174, v175 op_sel_hi:[0,0,0]
	v_mfma_scale_f32_16x16x128_f8f6f4 v[66:69], v[26:33], v[208:215], v[66:69], v174, v175 op_sel_hi:[0,0,0]
	s_mov_b32 m0, s79
	s_nop 0
	global_load_lds_dwordx4 v182, s[70:71]
	s_setprio 0
	s_setprio 1
	v_mfma_scale_f32_16x16x128_f8f6f4 v[62:65], v[2:9], v[184:191], v[62:65], v174, v175 op_sel_hi:[0,0,0]
	v_mfma_scale_f32_16x16x128_f8f6f4 v[58:61], v[10:17], v[184:191], v[58:61], v174, v175 op_sel_hi:[0,0,0]
	v_mfma_scale_f32_16x16x128_f8f6f4 v[54:57], v[2:9], v[192:199], v[54:57], v174, v175 op_sel_hi:[0,0,0]
	v_mfma_scale_f32_16x16x128_f8f6f4 v[50:53], v[10:17], v[192:199], v[50:53], v174, v175 op_sel_hi:[0,0,0]
	v_mfma_scale_f32_16x16x128_f8f6f4 v[46:49], v[2:9], v[200:207], v[46:49], v174, v175 op_sel_hi:[0,0,0]
	v_mfma_scale_f32_16x16x128_f8f6f4 v[42:45], v[10:17], v[200:207], v[42:45], v174, v175 op_sel_hi:[0,0,0]
	v_mfma_scale_f32_16x16x128_f8f6f4 v[38:41], v[2:9], v[208:215], v[38:41], v174, v175 op_sel_hi:[0,0,0]
	v_mfma_scale_f32_16x16x128_f8f6f4 v[34:37], v[10:17], v[208:215], v[34:37], v174, v175 op_sel_hi:[0,0,0]
	s_setprio 0
	s_barrier
; #define PG8_STAGE(bufoff, gbase, voff) do { _Pragma("unroll") for (int _i = 0; _i < 2; ++_i) \
;         asm volatile("s_mov_b32 m0, %0\n\ts_nop 0\n\tglobal_load_lds_dwordx4 %1, %2" :: "s"(ldsb + (unsigned)(bufoff) + ldsw + _i * 8192u), "v"((voff)[_i]), "s"((const char*)(gbase)) : "m0", "memory"); } while (0)
; #define PG8_WAIT_V(n) asm volatile("s_waitcnt vmcnt(" #n ")" ::: "memory")
; #define PG8_WAIT_L(n) asm volatile("s_waitcnt lgkmcnt(" #n ")" ::: "memory")
; #define PG8_BAR __builtin_amdgcn_s_barrier()
; #define PG8_SCHED __builtin_amdgcn_sched_barrier(0)
; template <class Epi, class Sched, bool F8 = false, bool MID = false, bool GATHER = false>
; __device__ __forceinline__ void gemm_phase(LAS unsigned char* lds, const Gemm g, const Sched& S, const Epi& E) {
;     ...
;             PG8_LDB(B0, 1, 0); PG8_LDB(B1, 1, 1); PG8_SCHED; PG8_LDA(At, 1, 0); PG8_STAGE(PG8_SA(0, 1), a2, xA1);
;             PG8_WAIT_V(8); PG8_WAIT_L(0); PG8_BAR; PG8_MMA(0, 0, At, B0); PG8_MMA(0, 1, At, B1); PG8_BAR; PG8_SCHED;
;             PG8_LDA(At, 1, 1); PG8_STAGE(PG8_SB(1, 0), b3, voffB); PG8_STAGE(PG8_SB(1, 1), b3 + hstepB, voffB); PG8_STAGE(PG8_SA(1, 0), a3, xA0);
;             PG8_WAIT_V(8); PG8_WAIT_L(0); PG8_BAR; PG8_MMA(1, 0, At, B0); PG8_MMA(1, 1, At, B1); PG8_BAR; PG8_SCHED;
;         }
	v_add_u32_e32 v14, 0x18000, v172
	v_add_u32_e32 v30, 0x1c000, v172
	ds_read_b128 v[2:5], v14
	ds_read_b128 v[6:9], v14 offset:1024
	ds_read_b128 v[10:13], v14 offset:2048
	ds_read_b128 v[14:17], v14 offset:3072
	ds_read_b128 v[18:21], v30
	ds_read_b128 v[22:25], v30 offset:1024
	ds_read_b128 v[26:29], v30 offset:2048
	ds_read_b128 v[30:33], v30 offset:3072
	ds_read_b128 v[184:187], v173 offset:32768
	ds_read_b128 v[188:191], v173 offset:33792
	ds_read_b128 v[192:195], v173 offset:34816
	ds_read_b128 v[196:199], v173 offset:35840
	ds_read_b128 v[200:203], v173 offset:36864
	ds_read_b128 v[204:207], v173 offset:37888
	ds_read_b128 v[208:211], v173 offset:38912
	ds_read_b128 v[212:215], v173 offset:39936
	s_mov_b32 m0, s85
	s_nop 0
	global_load_lds_dwordx4 v183, s[70:71]
	s_nop 0
	s_mov_b32 m0, s86
	s_nop 0
	global_load_lds_dwordx4 v216, s[70:71]
	s_waitcnt vmcnt(8)
	s_waitcnt lgkmcnt(0)
	s_barrier
	s_setprio 1
	s_waitcnt lgkmcnt(6)
	v_mfma_scale_f32_16x16x128_f8f6f4 v[158:161], v[2:9], v[184:191], v[158:161], v174, v175 op_sel_hi:[0,0,0]
	v_mfma_scale_f32_16x16x128_f8f6f4 v[154:157], v[10:17], v[184:191], v[154:157], v174, v175 op_sel_hi:[0,0,0]
	s_waitcnt lgkmcnt(4)
	v_mfma_scale_f32_16x16x128_f8f6f4 v[150:153], v[2:9], v[192:199], v[150:153], v174, v175 op_sel_hi:[0,0,0]
	v_mfma_scale_f32_16x16x128_f8f6f4 v[146:149], v[10:17], v[192:199], v[146:149], v174, v175 op_sel_hi:[0,0,0]
	s_waitcnt lgkmcnt(2)
	v_mfma_scale_f32_16x16x128_f8f6f4 v[142:145], v[2:9], v[200:207], v[142:145], v174, v175 op_sel_hi:[0,0,0]
	v_mfma_scale_f32_16x16x128_f8f6f4 v[138:141], v[10:17], v[200:207], v[138:141], v174, v175 op_sel_hi:[0,0,0]
	s_waitcnt lgkmcnt(0)
	v_mfma_scale_f32_16x16x128_f8f6f4 v[134:137], v[2:9], v[208:215], v[134:137], v174, v175 op_sel_hi:[0,0,0]
	v_mfma_scale_f32_16x16x128_f8f6f4 v[130:133], v[10:17], v[208:215], v[130:133], v174, v175 op_sel_hi:[0,0,0]
	s_setprio 0
	s_setprio 1
	v_mfma_scale_f32_16x16x128_f8f6f4 v[126:129], v[18:25], v[184:191], v[126:129], v174, v175 op_sel_hi:[0,0,0]
	v_mfma_scale_f32_16x16x128_f8f6f4 v[122:125], v[26:33], v[184:191], v[122:125], v174, v175 op_sel_hi:[0,0,0]
	v_mfma_scale_f32_16x16x128_f8f6f4 v[118:121], v[18:25], v[192:199], v[118:121], v174, v175 op_sel_hi:[0,0,0]
	v_mfma_scale_f32_16x16x128_f8f6f4 v[114:117], v[26:33], v[192:199], v[114:117], v174, v175 op_sel_hi:[0,0,0]
	v_mfma_scale_f32_16x16x128_f8f6f4 v[110:113], v[18:25], v[200:207], v[110:113], v174, v175 op_sel_hi:[0,0,0]
	v_mfma_scale_f32_16x16x128_f8f6f4 v[106:109], v[26:33], v[200:207], v[106:109], v174, v175 op_sel_hi:[0,0,0]
	v_mfma_scale_f32_16x16x128_f8f6f4 v[102:105], v[18:25], v[208:215], v[102:105], v174, v175 op_sel_hi:[0,0,0]
	v_mfma_scale_f32_16x16x128_f8f6f4 v[98:101], v[26:33], v[208:215], v[98:101], v174, v175 op_sel_hi:[0,0,0]
	s_setprio 0
	s_barrier
	ds_read_b128 v[184:187], v173 offset:49152
	ds_read_b128 v[188:191], v173 offset:50176
	ds_read_b128 v[192:195], v173 offset:51200
	ds_read_b128 v[196:199], v173 offset:52224
	ds_read_b128 v[200:203], v173 offset:53248
	ds_read_b128 v[204:207], v173 offset:54272
	ds_read_b128 v[208:211], v173 offset:55296
	ds_read_b128 v[212:215], v173 offset:56320
	s_add_u32 s22, s66, 0x80
	s_addc_u32 s23, s67, 0
	s_mov_b32 m0, s89
	s_nop 0
	global_load_lds_dwordx4 v163, s[22:23]
	s_nop 0
	s_mov_b32 m0, s90
	s_nop 0
	global_load_lds_dwordx4 v167, s[22:23]
	s_add_u32 s22, s66, 0x40080
	s_addc_u32 s23, s67, 0
	s_waitcnt vmcnt(4)
	s_waitcnt lgkmcnt(0)
	s_barrier
	s_setprio 1
	s_waitcnt lgkmcnt(6)
	v_mfma_scale_f32_16x16x128_f8f6f4 v[94:97], v[2:9], v[184:191], v[94:97], v174, v175 op_sel_hi:[0,0,0]
	v_mfma_scale_f32_16x16x128_f8f6f4 v[90:93], v[10:17], v[184:191], v[90:93], v174, v175 op_sel_hi:[0,0,0]
	s_mov_b32 m0, s93
	s_nop 0
	global_load_lds_dwordx4 v163, s[22:23]
	s_waitcnt lgkmcnt(4)
	v_mfma_scale_f32_16x16x128_f8f6f4 v[86:89], v[2:9], v[192:199], v[86:89], v174, v175 op_sel_hi:[0,0,0]
	v_mfma_scale_f32_16x16x128_f8f6f4 v[82:85], v[10:17], v[192:199], v[82:85], v174, v175 op_sel_hi:[0,0,0]
	s_mov_b32 m0, s94
	s_nop 0
	global_load_lds_dwordx4 v167, s[22:23]
	s_waitcnt lgkmcnt(2)
	v_mfma_scale_f32_16x16x128_f8f6f4 v[78:81], v[2:9], v[200:207], v[78:81], v174, v175 op_sel_hi:[0,0,0]
	v_mfma_scale_f32_16x16x128_f8f6f4 v[74:77], v[10:17], v[200:207], v[74:77], v174, v175 op_sel_hi:[0,0,0]
	s_mov_b32 m0, s91
	s_nop 0
	global_load_lds_dwordx4 v181, s[68:69]
	s_waitcnt lgkmcnt(0)
	v_mfma_scale_f32_16x16x128_f8f6f4 v[70:73], v[2:9], v[208:215], v[70:73], v174, v175 op_sel_hi:[0,0,0]
	v_mfma_scale_f32_16x16x128_f8f6f4 v[66:69], v[10:17], v[208:215], v[66:69], v174, v175 op_sel_hi:[0,0,0]
	s_mov_b32 m0, s92
	s_nop 0
	global_load_lds_dwordx4 v182, s[68:69]
	s_setprio 0
	s_setprio 1
	v_mfma_scale_f32_16x16x128_f8f6f4 v[62:65], v[18:25], v[184:191], v[62:65], v174, v175 op_sel_hi:[0,0,0]
	v_mfma_scale_f32_16x16x128_f8f6f4 v[58:61], v[26:33], v[184:191], v[58:61], v174, v175 op_sel_hi:[0,0,0]
	v_mfma_scale_f32_16x16x128_f8f6f4 v[54:57], v[18:25], v[192:199], v[54:57], v174, v175 op_sel_hi:[0,0,0]
	v_mfma_scale_f32_16x16x128_f8f6f4 v[50:53], v[26:33], v[192:199], v[50:53], v174, v175 op_sel_hi:[0,0,0]
	v_mfma_scale_f32_16x16x128_f8f6f4 v[46:49], v[18:25], v[200:207], v[46:49], v174, v175 op_sel_hi:[0,0,0]
	v_mfma_scale_f32_16x16x128_f8f6f4 v[42:45], v[26:33], v[200:207], v[42:45], v174, v175 op_sel_hi:[0,0,0]
	v_mfma_scale_f32_16x16x128_f8f6f4 v[38:41], v[18:25], v[208:215], v[38:41], v174, v175 op_sel_hi:[0,0,0]
	v_mfma_scale_f32_16x16x128_f8f6f4 v[34:37], v[26:33], v[208:215], v[34:37], v174, v175 op_sel_hi:[0,0,0]
	s_setprio 0
	s_barrier
	s_add_i32 s13, s13, 2
	s_add_u32 s64, s64, 0x100
	s_addc_u32 s65, s65, 0
	s_cmp_gt_u32 s13, 13
	s_cbranch_scc0 .LBB0_2474
	s_and_b64 vcc, exec, s[54:55]
	s_cbranch_vccz .LBB0_2477
	s_barrier

; #define PG8_STAGE(bufoff, gbase, voff) do { _Pragma("unroll") for (int _i = 0; _i < 2; ++_i) \
;         asm volatile("s_mov_b32 m0, %0\n\ts_nop 0\n\tglobal_load_lds_dwordx4 %1, %2" :: "s"(ldsb + (unsigned)(bufoff) + ldsw + _i * 8192u), "v"((voff)[_i]), "s"((const char*)(gbase)) : "m0", "memory"); } while (0)
; #define PG8_WAIT_V(n) asm volatile("s_waitcnt vmcnt(" #n ")" ::: "memory")
; #define PG8_WAIT_L(n) asm volatile("s_waitcnt lgkmcnt(" #n ")" ::: "memory")
; #define PG8_BAR __builtin_amdgcn_s_barrier()
; #define PG8_SCHED __builtin_amdgcn_sched_barrier(0)
; template <class Epi, class Sched, bool F8 = false, bool MID = false, bool GATHER = false>
; __device__ __forceinline__ void gemm_phase(LAS unsigned char* lds, const Gemm g, const Sched& S, const Epi& E) {
;     ...
;         for (int t = 0; t < nt; t += 2) {
;             const bool last = (t == nt - 2);
;             const char* a1 = cA + (size_t)(t + 1) * kstep;
;             const char* a2 = last ? nA : cA + (size_t)(t + 2) * kstep; const char* b2 = last ? nB : cB + (size_t)(t + 2) * kstep;
;             const char* a3 = a2 + kstep; const char* b3 = b2 + kstep;
;             unsigned xA0[2], xA1[2];
; #pragma unroll
;             for (int i = 0; i < 2; ++i) { xA0[i] = last ? nvA0[i] : voffA[i]; xA1[i] = last ? nvA1[i] : voffA1[i]; }
;             if constexpr (MID) { if (t == (nt >> 1)) { if constexpr (F8) asm volatile("s_nop 15\n\ts_nop 15" ::: "memory"); int l_; asm volatile("v_mbcnt_lo_u32_b32 %0, -1, 0\n\tv_mbcnt_hi_u32_b32 %0, -1, %0" : "=v"(l_)); E.mid(acc, cur, wr, wc, l_ & 15, l_ >> 4); if constexpr (F8) asm volatile("s_nop 7" ::: "memory"); } }
;             PG8_LDB(B0, 0, 0); PG8_LDB(B1, 0, 1); PG8_SCHED; PG8_LDA(At, 0, 0); PG8_STAGE(PG8_SA(1, 1), a1, voffA1);
;             PG8_WAIT_V(8); PG8_WAIT_L(0); PG8_BAR; PG8_MMA(0, 0, At, B0); PG8_MMA(0, 1, At, B1); PG8_BAR; PG8_SCHED;
;             PG8_LDA(At, 0, 1); PG8_STAGE(PG8_SB(0, 0), b2, voffB); PG8_STAGE(PG8_SB(0, 1), b2 + hstepB, voffB); PG8_STAGE(PG8_SA(0, 0), a2, xA0);
;             PG8_WAIT_V(8); PG8_WAIT_L(0); PG8_BAR; PG8_MMA(1, 0, At, B0); PG8_MMA(1, 1, At, B1); PG8_BAR; PG8_SCHED;
.LBB0_2557:
	ds_read_b128 v[18:21], v169
	ds_read_b128 v[22:25], v169 offset:1024
	ds_read_b128 v[26:29], v169 offset:2048
	ds_read_b128 v[30:33], v169 offset:3072
	ds_read_b128 v[2:5], v170
	ds_read_b128 v[6:9], v170 offset:1024
	ds_read_b128 v[10:13], v170 offset:2048
	ds_read_b128 v[14:17], v170 offset:3072
	s_add_u32 s64, s66, 0x100
	s_addc_u32 s65, s67, 0
	s_cmp_eq_u32 vcc_lo, 12
	s_cselect_b32 s72, s56, s64
	s_cselect_b32 s73, s57, s65
	s_cselect_b32 s68, s58, s55
	s_cselect_b32 s69, s59, s97
	s_add_u32 s70, s72, 0x80
	s_addc_u32 s71, s73, 0
	s_add_u32 s22, s66, 0x80
	s_addc_u32 s23, s67, 0
	ds_read_b128 v[176:179], v171
	ds_read_b128 v[180:183], v171 offset:1024
	ds_read_b128 v[184:187], v171 offset:2048
	ds_read_b128 v[188:191], v171 offset:3072
	ds_read_b128 v[192:195], v171 offset:4096
	ds_read_b128 v[196:199], v171 offset:5120
	ds_read_b128 v[200:203], v171 offset:6144
	ds_read_b128 v[204:207], v171 offset:7168
	s_mov_b32 m0, s89
	s_nop 0
	global_load_lds_dwordx4 v162, s[22:23]
	s_nop 0
	s_mov_b32 m0, s90
	s_nop 0
	global_load_lds_dwordx4 v167, s[22:23]
	s_waitcnt vmcnt(8)
	s_waitcnt lgkmcnt(0)
	s_barrier
	s_setprio 1
	s_waitcnt lgkmcnt(0)
	v_mfma_scale_f32_16x16x128_f8f6f4 v[158:161], v[18:25], v[176:183], v[158:161], v172, v173 op_sel_hi:[0,0,0]
	v_mfma_scale_f32_16x16x128_f8f6f4 v[154:157], v[26:33], v[176:183], v[154:157], v172, v173 op_sel_hi:[0,0,0]
	v_mfma_scale_f32_16x16x128_f8f6f4 v[150:153], v[18:25], v[184:191], v[150:153], v172, v173 op_sel_hi:[0,0,0]
	v_mfma_scale_f32_16x16x128_f8f6f4 v[146:149], v[26:33], v[184:191], v[146:149], v172, v173 op_sel_hi:[0,0,0]
	v_mfma_scale_f32_16x16x128_f8f6f4 v[142:145], v[18:25], v[192:199], v[142:145], v172, v173 op_sel_hi:[0,0,0]
	v_mfma_scale_f32_16x16x128_f8f6f4 v[122:125], v[26:33], v[192:199], v[122:125], v172, v173 op_sel_hi:[0,0,0]
	v_mfma_scale_f32_16x16x128_f8f6f4 v[114:117], v[18:25], v[200:207], v[114:117], v172, v173 op_sel_hi:[0,0,0]
	v_mfma_scale_f32_16x16x128_f8f6f4 v[106:109], v[26:33], v[200:207], v[106:109], v172, v173 op_sel_hi:[0,0,0]
	s_setprio 0
	s_setprio 1
	v_mfma_scale_f32_16x16x128_f8f6f4 v[138:141], v[2:9], v[176:183], v[138:141], v172, v173 op_sel_hi:[0,0,0]
	v_mfma_scale_f32_16x16x128_f8f6f4 v[134:137], v[10:17], v[176:183], v[134:137], v172, v173 op_sel_hi:[0,0,0]
	v_mfma_scale_f32_16x16x128_f8f6f4 v[130:133], v[2:9], v[184:191], v[130:133], v172, v173 op_sel_hi:[0,0,0]
	v_mfma_scale_f32_16x16x128_f8f6f4 v[126:129], v[10:17], v[184:191], v[126:129], v172, v173 op_sel_hi:[0,0,0]
	v_mfma_scale_f32_16x16x128_f8f6f4 v[118:121], v[2:9], v[192:199], v[118:121], v172, v173 op_sel_hi:[0,0,0]
	v_mfma_scale_f32_16x16x128_f8f6f4 v[110:113], v[10:17], v[192:199], v[110:113], v172, v173 op_sel_hi:[0,0,0]
	v_mfma_scale_f32_16x16x128_f8f6f4 v[102:105], v[2:9], v[200:207], v[102:105], v172, v173 op_sel_hi:[0,0,0]
	v_mfma_scale_f32_16x16x128_f8f6f4 v[98:101], v[10:17], v[200:207], v[98:101], v172, v173 op_sel_hi:[0,0,0]
	s_setprio 0
	s_barrier
	ds_read_b128 v[176:179], v171 offset:16384
	ds_read_b128 v[180:183], v171 offset:17408
	ds_read_b128 v[184:187], v171 offset:18432
	ds_read_b128 v[188:191], v171 offset:19456
	ds_read_b128 v[192:195], v171 offset:20480
	ds_read_b128 v[196:199], v171 offset:21504
	ds_read_b128 v[200:203], v171 offset:22528
	ds_read_b128 v[204:207], v171 offset:23552
	s_mov_b32 m0, s26
	s_nop 0
	global_load_lds_dwordx4 v163, s[68:69]
	s_add_u32 s22, s68, 0x40000
	s_mov_b32 m0, s27
	s_nop 0
	global_load_lds_dwordx4 v168, s[68:69]
	s_addc_u32 s23, s69, 0
	s_waitcnt vmcnt(4)
	s_waitcnt lgkmcnt(0)
	s_barrier
	s_setprio 1
	s_waitcnt lgkmcnt(6)
	v_mfma_scale_f32_16x16x128_f8f6f4 v[94:97], v[18:25], v[176:183], v[94:97], v172, v173 op_sel_hi:[0,0,0]
	v_mfma_scale_f32_16x16x128_f8f6f4 v[90:93], v[26:33], v[176:183], v[90:93], v172, v173 op_sel_hi:[0,0,0]
	s_mov_b32 m0, s39
	s_nop 0
	global_load_lds_dwordx4 v163, s[22:23]
	s_waitcnt lgkmcnt(4)
	v_mfma_scale_f32_16x16x128_f8f6f4 v[82:85], v[18:25], v[184:191], v[82:85], v172, v173 op_sel_hi:[0,0,0]
	v_mfma_scale_f32_16x16x128_f8f6f4 v[70:73], v[26:33], v[184:191], v[70:73], v172, v173 op_sel_hi:[0,0,0]
	s_mov_b32 m0, s41
	s_nop 0
	global_load_lds_dwordx4 v168, s[22:23]
	s_waitcnt lgkmcnt(2)
	v_mfma_scale_f32_16x16x128_f8f6f4 v[54:57], v[18:25], v[192:199], v[54:57], v172, v173 op_sel_hi:[0,0,0]
	v_mfma_scale_f32_16x16x128_f8f6f4 v[42:45], v[26:33], v[192:199], v[42:45], v172, v173 op_sel_hi:[0,0,0]
	s_mov_b32 m0, s17
	s_nop 0
	global_load_lds_dwordx4 v1, s[72:73]
	s_waitcnt lgkmcnt(0)
	v_mfma_scale_f32_16x16x128_f8f6f4 v[38:41], v[18:25], v[200:207], v[38:41], v172, v173 op_sel_hi:[0,0,0]
	v_mfma_scale_f32_16x16x128_f8f6f4 v[34:37], v[26:33], v[200:207], v[34:37], v172, v173 op_sel_hi:[0,0,0]
	s_mov_b32 m0, s74
	s_nop 0
	global_load_lds_dwordx4 v165, s[72:73]
	s_setprio 0
	s_setprio 1
	v_mfma_scale_f32_16x16x128_f8f6f4 v[86:89], v[2:9], v[176:183], v[86:89], v172, v173 op_sel_hi:[0,0,0]
	v_mfma_scale_f32_16x16x128_f8f6f4 v[78:81], v[10:17], v[176:183], v[78:81], v172, v173 op_sel_hi:[0,0,0]
	v_mfma_scale_f32_16x16x128_f8f6f4 v[62:65], v[2:9], v[184:191], v[62:65], v172, v173 op_sel_hi:[0,0,0]
	v_mfma_scale_f32_16x16x128_f8f6f4 v[46:49], v[10:17], v[184:191], v[46:49], v172, v173 op_sel_hi:[0,0,0]
	v_mfma_scale_f32_16x16x128_f8f6f4 v[74:77], v[2:9], v[192:199], v[74:77], v172, v173 op_sel_hi:[0,0,0]
	v_mfma_scale_f32_16x16x128_f8f6f4 v[66:69], v[10:17], v[192:199], v[66:69], v172, v173 op_sel_hi:[0,0,0]
	v_mfma_scale_f32_16x16x128_f8f6f4 v[58:61], v[2:9], v[200:207], v[58:61], v172, v173 op_sel_hi:[0,0,0]
	v_mfma_scale_f32_16x16x128_f8f6f4 v[50:53], v[10:17], v[200:207], v[50:53], v172, v173 op_sel_hi:[0,0,0]
	s_setprio 0
	s_barrier
; #define PG8_STAGE(bufoff, gbase, voff) do { _Pragma("unroll") for (int _i = 0; _i < 2; ++_i) \
;         asm volatile("s_mov_b32 m0, %0\n\ts_nop 0\n\tglobal_load_lds_dwordx4 %1, %2" :: "s"(ldsb + (unsigned)(bufoff) + ldsw + _i * 8192u), "v"((voff)[_i]), "s"((const char*)(gbase)) : "m0", "memory"); } while (0)
; #define PG8_WAIT_V(n) asm volatile("s_waitcnt vmcnt(" #n ")" ::: "memory")
; #define PG8_WAIT_L(n) asm volatile("s_waitcnt lgkmcnt(" #n ")" ::: "memory")
; #define PG8_BAR __builtin_amdgcn_s_barrier()
; #define PG8_SCHED __builtin_amdgcn_sched_barrier(0)
; template <class Epi, class Sched, bool F8 = false, bool MID = false, bool GATHER = false>
; __device__ __forceinline__ void gemm_phase(LAS unsigned char* lds, const Gemm g, const Sched& S, const Epi& E) {
;     ...
;             PG8_LDB(B0, 1, 0); PG8_LDB(B1, 1, 1); PG8_SCHED; PG8_LDA(At, 1, 0); PG8_STAGE(PG8_SA(0, 1), a2, xA1);
;             PG8_WAIT_V(8); PG8_WAIT_L(0); PG8_BAR; PG8_MMA(0, 0, At, B0); PG8_MMA(0, 1, At, B1); PG8_BAR; PG8_SCHED;
;             PG8_LDA(At, 1, 1); PG8_STAGE(PG8_SB(1, 0), b3, voffB); PG8_STAGE(PG8_SB(1, 1), b3 + hstepB, voffB); PG8_STAGE(PG8_SA(1, 0), a3, xA0);
;             PG8_WAIT_V(8); PG8_WAIT_L(0); PG8_BAR; PG8_MMA(1, 0, At, B0); PG8_MMA(1, 1, At, B1); PG8_BAR; PG8_SCHED;
;         }
	ds_read_b128 v[2:5], v174
	ds_read_b128 v[6:9], v174 offset:1024
	ds_read_b128 v[10:13], v174 offset:2048
	ds_read_b128 v[14:17], v174 offset:3072
	ds_read_b128 v[18:21], v175
	ds_read_b128 v[22:25], v175 offset:1024
	ds_read_b128 v[26:29], v175 offset:2048
	ds_read_b128 v[30:33], v175 offset:3072
	ds_read_b128 v[176:179], v171 offset:32768
	ds_read_b128 v[180:183], v171 offset:33792
	ds_read_b128 v[184:187], v171 offset:34816
	ds_read_b128 v[188:191], v171 offset:35840
	ds_read_b128 v[192:195], v171 offset:36864
	ds_read_b128 v[196:199], v171 offset:37888
	ds_read_b128 v[200:203], v171 offset:38912
	ds_read_b128 v[204:207], v171 offset:39936
	s_mov_b32 m0, s75
	s_nop 0
	global_load_lds_dwordx4 v162, s[72:73]
	s_nop 0
	s_mov_b32 m0, s76
	s_nop 0
	global_load_lds_dwordx4 v167, s[72:73]
	s_waitcnt vmcnt(8)
	s_waitcnt lgkmcnt(0)
	s_barrier
	s_setprio 1
	s_waitcnt lgkmcnt(6)
	v_mfma_scale_f32_16x16x128_f8f6f4 v[158:161], v[2:9], v[176:183], v[158:161], v172, v173 op_sel_hi:[0,0,0]
	v_mfma_scale_f32_16x16x128_f8f6f4 v[154:157], v[10:17], v[176:183], v[154:157], v172, v173 op_sel_hi:[0,0,0]
	s_waitcnt lgkmcnt(4)
	v_mfma_scale_f32_16x16x128_f8f6f4 v[150:153], v[2:9], v[184:191], v[150:153], v172, v173 op_sel_hi:[0,0,0]
	v_mfma_scale_f32_16x16x128_f8f6f4 v[146:149], v[10:17], v[184:191], v[146:149], v172, v173 op_sel_hi:[0,0,0]
	s_waitcnt lgkmcnt(2)
	v_mfma_scale_f32_16x16x128_f8f6f4 v[142:145], v[2:9], v[192:199], v[142:145], v172, v173 op_sel_hi:[0,0,0]
	v_mfma_scale_f32_16x16x128_f8f6f4 v[122:125], v[10:17], v[192:199], v[122:125], v172, v173 op_sel_hi:[0,0,0]
	s_waitcnt lgkmcnt(0)
	v_mfma_scale_f32_16x16x128_f8f6f4 v[114:117], v[2:9], v[200:207], v[114:117], v172, v173 op_sel_hi:[0,0,0]
	v_mfma_scale_f32_16x16x128_f8f6f4 v[106:109], v[10:17], v[200:207], v[106:109], v172, v173 op_sel_hi:[0,0,0]
	s_setprio 0
	s_setprio 1
	v_mfma_scale_f32_16x16x128_f8f6f4 v[138:141], v[18:25], v[176:183], v[138:141], v172, v173 op_sel_hi:[0,0,0]
	v_mfma_scale_f32_16x16x128_f8f6f4 v[134:137], v[26:33], v[176:183], v[134:137], v172, v173 op_sel_hi:[0,0,0]
	v_mfma_scale_f32_16x16x128_f8f6f4 v[130:133], v[18:25], v[184:191], v[130:133], v172, v173 op_sel_hi:[0,0,0]
	v_mfma_scale_f32_16x16x128_f8f6f4 v[126:129], v[26:33], v[184:191], v[126:129], v172, v173 op_sel_hi:[0,0,0]
	v_mfma_scale_f32_16x16x128_f8f6f4 v[118:121], v[18:25], v[192:199], v[118:121], v172, v173 op_sel_hi:[0,0,0]
	v_mfma_scale_f32_16x16x128_f8f6f4 v[110:113], v[26:33], v[192:199], v[110:113], v172, v173 op_sel_hi:[0,0,0]
	v_mfma_scale_f32_16x16x128_f8f6f4 v[102:105], v[18:25], v[200:207], v[102:105], v172, v173 op_sel_hi:[0,0,0]
	v_mfma_scale_f32_16x16x128_f8f6f4 v[98:101], v[26:33], v[200:207], v[98:101], v172, v173 op_sel_hi:[0,0,0]
	s_setprio 0
	s_barrier
	ds_read_b128 v[176:179], v171 offset:49152
	ds_read_b128 v[180:183], v171 offset:50176
	ds_read_b128 v[184:187], v171 offset:51200
	ds_read_b128 v[188:191], v171 offset:52224
	ds_read_b128 v[192:195], v171 offset:53248
	ds_read_b128 v[196:199], v171 offset:54272
	ds_read_b128 v[200:203], v171 offset:55296
	ds_read_b128 v[204:207], v171 offset:56320
	s_add_u32 s22, s68, 0x80
	s_addc_u32 s23, s69, 0
	s_mov_b32 m0, s80
	s_nop 0
	global_load_lds_dwordx4 v163, s[22:23]
	s_nop 0
	s_mov_b32 m0, s81
	s_nop 0
	global_load_lds_dwordx4 v168, s[22:23]
	s_add_u32 s22, s68, 0x40080
	s_addc_u32 s23, s69, 0
	s_waitcnt vmcnt(4)
	s_waitcnt lgkmcnt(0)
	s_barrier
	s_setprio 1
	s_waitcnt lgkmcnt(6)
	v_mfma_scale_f32_16x16x128_f8f6f4 v[94:97], v[2:9], v[176:183], v[94:97], v172, v173 op_sel_hi:[0,0,0]
	v_mfma_scale_f32_16x16x128_f8f6f4 v[90:93], v[10:17], v[176:183], v[90:93], v172, v173 op_sel_hi:[0,0,0]
	s_mov_b32 m0, s87
	s_nop 0
	global_load_lds_dwordx4 v163, s[22:23]
	s_waitcnt lgkmcnt(4)
	v_mfma_scale_f32_16x16x128_f8f6f4 v[82:85], v[2:9], v[184:191], v[82:85], v172, v173 op_sel_hi:[0,0,0]
	v_mfma_scale_f32_16x16x128_f8f6f4 v[70:73], v[10:17], v[184:191], v[70:73], v172, v173 op_sel_hi:[0,0,0]
	s_mov_b32 m0, s88
	s_nop 0
	global_load_lds_dwordx4 v168, s[22:23]
	s_waitcnt lgkmcnt(2)
	v_mfma_scale_f32_16x16x128_f8f6f4 v[54:57], v[2:9], v[192:199], v[54:57], v172, v173 op_sel_hi:[0,0,0]
	v_mfma_scale_f32_16x16x128_f8f6f4 v[42:45], v[10:17], v[192:199], v[42:45], v172, v173 op_sel_hi:[0,0,0]
	s_mov_b32 m0, s85
	s_nop 0
	global_load_lds_dwordx4 v1, s[70:71]
	s_waitcnt lgkmcnt(0)
	v_mfma_scale_f32_16x16x128_f8f6f4 v[38:41], v[2:9], v[200:207], v[38:41], v172, v173 op_sel_hi:[0,0,0]
	v_mfma_scale_f32_16x16x128_f8f6f4 v[34:37], v[10:17], v[200:207], v[34:37], v172, v173 op_sel_hi:[0,0,0]
	s_mov_b32 m0, s86
	s_nop 0
	global_load_lds_dwordx4 v165, s[70:71]
	s_setprio 0
	s_setprio 1
	v_mfma_scale_f32_16x16x128_f8f6f4 v[86:89], v[18:25], v[176:183], v[86:89], v172, v173 op_sel_hi:[0,0,0]
	v_mfma_scale_f32_16x16x128_f8f6f4 v[78:81], v[26:33], v[176:183], v[78:81], v172, v173 op_sel_hi:[0,0,0]
	v_mfma_scale_f32_16x16x128_f8f6f4 v[62:65], v[18:25], v[184:191], v[62:65], v172, v173 op_sel_hi:[0,0,0]
	v_mfma_scale_f32_16x16x128_f8f6f4 v[46:49], v[26:33], v[184:191], v[46:49], v172, v173 op_sel_hi:[0,0,0]
	v_mfma_scale_f32_16x16x128_f8f6f4 v[74:77], v[18:25], v[192:199], v[74:77], v172, v173 op_sel_hi:[0,0,0]
	v_mfma_scale_f32_16x16x128_f8f6f4 v[66:69], v[26:33], v[192:199], v[66:69], v172, v173 op_sel_hi:[0,0,0]
	v_mfma_scale_f32_16x16x128_f8f6f4 v[58:61], v[18:25], v[200:207], v[58:61], v172, v173 op_sel_hi:[0,0,0]
	v_mfma_scale_f32_16x16x128_f8f6f4 v[50:53], v[26:33], v[200:207], v[50:53], v172, v173 op_sel_hi:[0,0,0]
	s_setprio 0
	s_barrier
	s_add_i32 vcc_lo, vcc_lo, 2
	s_add_u32 s55, s55, 0x100
	s_addc_u32 s97, s97, 0
	s_cmp_gt_u32 vcc_lo, 13
	s_mov_b64 s[66:67], s[64:65]
	s_cbranch_scc0 .LBB0_2557
	s_and_b64 vcc, exec, s[12:13]
	s_cbranch_vccz .LBB0_2560
	s_barrier

; #define PG8_STAGE(bufoff, gbase, voff) do { _Pragma("unroll") for (int _i = 0; _i < 2; ++_i) \
;         asm volatile("s_mov_b32 m0, %0\n\ts_nop 0\n\tglobal_load_lds_dwordx4 %1, %2" :: "s"(ldsb + (unsigned)(bufoff) + ldsw + _i * 8192u), "v"((voff)[_i]), "s"((const char*)(gbase)) : "m0", "memory"); } while (0)
; #define PG8_WAIT_V(n) asm volatile("s_waitcnt vmcnt(" #n ")" ::: "memory")
; #define PG8_WAIT_L(n) asm volatile("s_waitcnt lgkmcnt(" #n ")" ::: "memory")
; #define PG8_BAR __builtin_amdgcn_s_barrier()
; #define PG8_SCHED __builtin_amdgcn_sched_barrier(0)
; template <class Epi, class Sched, bool F8 = false, bool MID = false, bool GATHER = false>
; __device__ __forceinline__ void gemm_phase(LAS unsigned char* lds, const Gemm g, const Sched& S, const Epi& E) {
;     ...
;         for (int t = 0; t < nt; t += 2) {
;             const bool last = (t == nt - 2);
;             const char* a1 = cA + (size_t)(t + 1) * kstep;
;             const char* a2 = last ? nA : cA + (size_t)(t + 2) * kstep; const char* b2 = last ? nB : cB + (size_t)(t + 2) * kstep;
;             const char* a3 = a2 + kstep; const char* b3 = b2 + kstep;
;             unsigned xA0[2], xA1[2];
; #pragma unroll
;             for (int i = 0; i < 2; ++i) { xA0[i] = last ? nvA0[i] : voffA[i]; xA1[i] = last ? nvA1[i] : voffA1[i]; }
;             if constexpr (MID) { if (t == (nt >> 1)) { if constexpr (F8) asm volatile("s_nop 15\n\ts_nop 15" ::: "memory"); int l_; asm volatile("v_mbcnt_lo_u32_b32 %0, -1, 0\n\tv_mbcnt_hi_u32_b32 %0, -1, %0" : "=v"(l_)); E.mid(acc, cur, wr, wc, l_ & 15, l_ >> 4); if constexpr (F8) asm volatile("s_nop 7" ::: "memory"); } }
;             PG8_LDB(B0, 0, 0); PG8_LDB(B1, 0, 1); PG8_SCHED; PG8_LDA(At, 0, 0); PG8_STAGE(PG8_SA(1, 1), a1, voffA1);
;             PG8_WAIT_V(8); PG8_WAIT_L(0); PG8_BAR; PG8_MMA(0, 0, At, B0); PG8_MMA(0, 1, At, B1); PG8_BAR; PG8_SCHED;
;             PG8_LDA(At, 0, 1); PG8_STAGE(PG8_SB(0, 0), b2, voffB); PG8_STAGE(PG8_SB(0, 1), b2 + hstepB, voffB); PG8_STAGE(PG8_SA(0, 0), a2, xA0);
;             PG8_WAIT_V(8); PG8_WAIT_L(0); PG8_BAR; PG8_MMA(1, 0, At, B0); PG8_MMA(1, 1, At, B1); PG8_BAR; PG8_SCHED;
.LBB0_2753:
	ds_read_b128 v[16:19], v166
	ds_read_b128 v[20:23], v166 offset:1024
	ds_read_b128 v[24:27], v166 offset:2048
	ds_read_b128 v[28:31], v166 offset:3072
	ds_read_b128 v[0:3], v168
	ds_read_b128 v[4:7], v168 offset:1024
	ds_read_b128 v[8:11], v168 offset:2048
	ds_read_b128 v[12:15], v168 offset:3072
	s_add_u32 s48, s50, 0x100
	s_addc_u32 s49, s51, 0
	s_cmp_eq_u32 s90, 12
	s_cselect_b32 s56, s44, s48
	s_cselect_b32 s57, s45, s49
	s_cselect_b32 s52, s46, s88
	s_cselect_b32 s53, s47, s89
	s_add_u32 s54, s56, 0x80
	s_addc_u32 s55, s57, 0
	s_add_u32 s22, s50, 0x80
	s_addc_u32 s23, s51, 0
	ds_read_b128 v[174:177], v169
	ds_read_b128 v[178:181], v169 offset:1024
	ds_read_b128 v[182:185], v169 offset:2048
	ds_read_b128 v[186:189], v169 offset:3072
	ds_read_b128 v[190:193], v169 offset:4096
	ds_read_b128 v[194:197], v169 offset:5120
	ds_read_b128 v[198:201], v169 offset:6144
	ds_read_b128 v[202:205], v169 offset:7168
	s_mov_b32 m0, s75
	s_nop 0
	global_load_lds_dwordx4 v161, s[22:23]
	s_nop 0
	s_mov_b32 m0, s76
	s_nop 0
	global_load_lds_dwordx4 v165, s[22:23]
	s_waitcnt vmcnt(8)
	s_waitcnt lgkmcnt(0)
	s_barrier
	s_setprio 1
	s_waitcnt lgkmcnt(6)
	v_mfma_scale_f32_16x16x128_f8f6f4 v[156:159], v[16:23], v[174:181], v[156:159], v170, v171 op_sel_hi:[0,0,0]
	v_mfma_scale_f32_16x16x128_f8f6f4 v[152:155], v[24:31], v[174:181], v[152:155], v170, v171 op_sel_hi:[0,0,0]
	s_waitcnt lgkmcnt(4)
	v_mfma_scale_f32_16x16x128_f8f6f4 v[140:143], v[16:23], v[182:189], v[140:143], v170, v171 op_sel_hi:[0,0,0]
	v_mfma_scale_f32_16x16x128_f8f6f4 v[136:139], v[24:31], v[182:189], v[136:139], v170, v171 op_sel_hi:[0,0,0]
	s_waitcnt lgkmcnt(2)
	v_mfma_scale_f32_16x16x128_f8f6f4 v[124:127], v[16:23], v[190:197], v[124:127], v170, v171 op_sel_hi:[0,0,0]
	v_mfma_scale_f32_16x16x128_f8f6f4 v[120:123], v[24:31], v[190:197], v[120:123], v170, v171 op_sel_hi:[0,0,0]
	s_waitcnt lgkmcnt(0)
	v_mfma_scale_f32_16x16x128_f8f6f4 v[108:111], v[16:23], v[198:205], v[108:111], v170, v171 op_sel_hi:[0,0,0]
	v_mfma_scale_f32_16x16x128_f8f6f4 v[104:107], v[24:31], v[198:205], v[104:107], v170, v171 op_sel_hi:[0,0,0]
	s_setprio 0
	s_setprio 1
	v_mfma_scale_f32_16x16x128_f8f6f4 v[148:151], v[0:7], v[174:181], v[148:151], v170, v171 op_sel_hi:[0,0,0]
	v_mfma_scale_f32_16x16x128_f8f6f4 v[144:147], v[8:15], v[174:181], v[144:147], v170, v171 op_sel_hi:[0,0,0]
	v_mfma_scale_f32_16x16x128_f8f6f4 v[132:135], v[0:7], v[182:189], v[132:135], v170, v171 op_sel_hi:[0,0,0]
	v_mfma_scale_f32_16x16x128_f8f6f4 v[128:131], v[8:15], v[182:189], v[128:131], v170, v171 op_sel_hi:[0,0,0]
	v_mfma_scale_f32_16x16x128_f8f6f4 v[116:119], v[0:7], v[190:197], v[116:119], v170, v171 op_sel_hi:[0,0,0]
	v_mfma_scale_f32_16x16x128_f8f6f4 v[112:115], v[8:15], v[190:197], v[112:115], v170, v171 op_sel_hi:[0,0,0]
	v_mfma_scale_f32_16x16x128_f8f6f4 v[100:103], v[0:7], v[198:205], v[100:103], v170, v171 op_sel_hi:[0,0,0]
	v_mfma_scale_f32_16x16x128_f8f6f4 v[96:99], v[8:15], v[198:205], v[96:99], v170, v171 op_sel_hi:[0,0,0]
	s_setprio 0
	s_barrier
	ds_read_b128 v[174:177], v169 offset:16384
	ds_read_b128 v[178:181], v169 offset:17408
	ds_read_b128 v[182:185], v169 offset:18432
	ds_read_b128 v[186:189], v169 offset:19456
	ds_read_b128 v[190:193], v169 offset:20480
	ds_read_b128 v[194:197], v169 offset:21504
	ds_read_b128 v[198:201], v169 offset:22528
	ds_read_b128 v[202:205], v169 offset:23552
	s_mov_b32 m0, s60
	s_nop 0
	global_load_lds_dwordx4 v162, s[52:53]
	s_add_u32 s22, s52, 0x40000
	s_mov_b32 m0, s61
	s_nop 0
	global_load_lds_dwordx4 v167, s[52:53]
	s_addc_u32 s23, s53, 0
	s_waitcnt vmcnt(4)
	s_waitcnt lgkmcnt(0)
	s_barrier
	s_setprio 1
	s_waitcnt lgkmcnt(6)
	v_mfma_scale_f32_16x16x128_f8f6f4 v[92:95], v[16:23], v[174:181], v[92:95], v170, v171 op_sel_hi:[0,0,0]
	v_mfma_scale_f32_16x16x128_f8f6f4 v[88:91], v[24:31], v[174:181], v[88:91], v170, v171 op_sel_hi:[0,0,0]
	s_mov_b32 m0, s62
	s_nop 0
	global_load_lds_dwordx4 v162, s[22:23]
	s_waitcnt lgkmcnt(4)
	v_mfma_scale_f32_16x16x128_f8f6f4 v[76:79], v[16:23], v[182:189], v[76:79], v170, v171 op_sel_hi:[0,0,0]
	v_mfma_scale_f32_16x16x128_f8f6f4 v[72:75], v[24:31], v[182:189], v[72:75], v170, v171 op_sel_hi:[0,0,0]
	s_mov_b32 m0, s63
	s_nop 0
	global_load_lds_dwordx4 v167, s[22:23]
	s_waitcnt lgkmcnt(2)
	v_mfma_scale_f32_16x16x128_f8f6f4 v[52:55], v[16:23], v[190:197], v[52:55], v170, v171 op_sel_hi:[0,0,0]
	v_mfma_scale_f32_16x16x128_f8f6f4 v[48:51], v[24:31], v[190:197], v[48:51], v170, v171 op_sel_hi:[0,0,0]
	s_mov_b32 m0, s58
	s_nop 0
	global_load_lds_dwordx4 v160, s[56:57]
	s_waitcnt lgkmcnt(0)
	v_mfma_scale_f32_16x16x128_f8f6f4 v[36:39], v[16:23], v[198:205], v[36:39], v170, v171 op_sel_hi:[0,0,0]
	v_mfma_scale_f32_16x16x128_f8f6f4 v[32:35], v[24:31], v[198:205], v[32:35], v170, v171 op_sel_hi:[0,0,0]
	s_mov_b32 m0, s64
	s_nop 0
	global_load_lds_dwordx4 v163, s[56:57]
	s_setprio 0
	s_setprio 1
	v_mfma_scale_f32_16x16x128_f8f6f4 v[84:87], v[0:7], v[174:181], v[84:87], v170, v171 op_sel_hi:[0,0,0]
	v_mfma_scale_f32_16x16x128_f8f6f4 v[80:83], v[8:15], v[174:181], v[80:83], v170, v171 op_sel_hi:[0,0,0]
	v_mfma_scale_f32_16x16x128_f8f6f4 v[68:71], v[0:7], v[182:189], v[68:71], v170, v171 op_sel_hi:[0,0,0]
	v_mfma_scale_f32_16x16x128_f8f6f4 v[56:59], v[8:15], v[182:189], v[56:59], v170, v171 op_sel_hi:[0,0,0]
	v_mfma_scale_f32_16x16x128_f8f6f4 v[64:67], v[0:7], v[190:197], v[64:67], v170, v171 op_sel_hi:[0,0,0]
	v_mfma_scale_f32_16x16x128_f8f6f4 v[60:63], v[8:15], v[190:197], v[60:63], v170, v171 op_sel_hi:[0,0,0]
	v_mfma_scale_f32_16x16x128_f8f6f4 v[44:47], v[0:7], v[198:205], v[44:47], v170, v171 op_sel_hi:[0,0,0]
	v_mfma_scale_f32_16x16x128_f8f6f4 v[40:43], v[8:15], v[198:205], v[40:43], v170, v171 op_sel_hi:[0,0,0]
	s_setprio 0
	s_barrier
; #define PG8_STAGE(bufoff, gbase, voff) do { _Pragma("unroll") for (int _i = 0; _i < 2; ++_i) \
;         asm volatile("s_mov_b32 m0, %0\n\ts_nop 0\n\tglobal_load_lds_dwordx4 %1, %2" :: "s"(ldsb + (unsigned)(bufoff) + ldsw + _i * 8192u), "v"((voff)[_i]), "s"((const char*)(gbase)) : "m0", "memory"); } while (0)
; #define PG8_WAIT_V(n) asm volatile("s_waitcnt vmcnt(" #n ")" ::: "memory")
; #define PG8_WAIT_L(n) asm volatile("s_waitcnt lgkmcnt(" #n ")" ::: "memory")
; #define PG8_BAR __builtin_amdgcn_s_barrier()
; #define PG8_SCHED __builtin_amdgcn_sched_barrier(0)
; template <class Epi, class Sched, bool F8 = false, bool MID = false, bool GATHER = false>
; __device__ __forceinline__ void gemm_phase(LAS unsigned char* lds, const Gemm g, const Sched& S, const Epi& E) {
;     ...
;             PG8_LDB(B0, 1, 0); PG8_LDB(B1, 1, 1); PG8_SCHED; PG8_LDA(At, 1, 0); PG8_STAGE(PG8_SA(0, 1), a2, xA1);
;             PG8_WAIT_V(8); PG8_WAIT_L(0); PG8_BAR; PG8_MMA(0, 0, At, B0); PG8_MMA(0, 1, At, B1); PG8_BAR; PG8_SCHED;
;             PG8_LDA(At, 1, 1); PG8_STAGE(PG8_SB(1, 0), b3, voffB); PG8_STAGE(PG8_SB(1, 1), b3 + hstepB, voffB); PG8_STAGE(PG8_SA(1, 0), a3, xA0);
;             PG8_WAIT_V(8); PG8_WAIT_L(0); PG8_BAR; PG8_MMA(1, 0, At, B0); PG8_MMA(1, 1, At, B1); PG8_BAR; PG8_SCHED;
;         }
	ds_read_b128 v[0:3], v172
	ds_read_b128 v[4:7], v172 offset:1024
	ds_read_b128 v[8:11], v172 offset:2048
	ds_read_b128 v[12:15], v172 offset:3072
	ds_read_b128 v[16:19], v173
	ds_read_b128 v[20:23], v173 offset:1024
	ds_read_b128 v[24:27], v173 offset:2048
	ds_read_b128 v[28:31], v173 offset:3072
	ds_read_b128 v[174:177], v169 offset:32768
	ds_read_b128 v[178:181], v169 offset:33792
	ds_read_b128 v[182:185], v169 offset:34816
	ds_read_b128 v[186:189], v169 offset:35840
	ds_read_b128 v[190:193], v169 offset:36864
	ds_read_b128 v[194:197], v169 offset:37888
	ds_read_b128 v[198:201], v169 offset:38912
	ds_read_b128 v[202:205], v169 offset:39936
	s_mov_b32 m0, s65
	s_nop 0
	global_load_lds_dwordx4 v161, s[56:57]
	s_nop 0
	s_mov_b32 m0, s66
	s_nop 0
	global_load_lds_dwordx4 v165, s[56:57]
	s_waitcnt vmcnt(8)
	s_waitcnt lgkmcnt(0)
	s_barrier
	s_setprio 1
	s_waitcnt lgkmcnt(6)
	v_mfma_scale_f32_16x16x128_f8f6f4 v[156:159], v[0:7], v[174:181], v[156:159], v170, v171 op_sel_hi:[0,0,0]
	v_mfma_scale_f32_16x16x128_f8f6f4 v[152:155], v[8:15], v[174:181], v[152:155], v170, v171 op_sel_hi:[0,0,0]
	s_waitcnt lgkmcnt(4)
	v_mfma_scale_f32_16x16x128_f8f6f4 v[140:143], v[0:7], v[182:189], v[140:143], v170, v171 op_sel_hi:[0,0,0]
	v_mfma_scale_f32_16x16x128_f8f6f4 v[136:139], v[8:15], v[182:189], v[136:139], v170, v171 op_sel_hi:[0,0,0]
	s_waitcnt lgkmcnt(2)
	v_mfma_scale_f32_16x16x128_f8f6f4 v[124:127], v[0:7], v[190:197], v[124:127], v170, v171 op_sel_hi:[0,0,0]
	v_mfma_scale_f32_16x16x128_f8f6f4 v[120:123], v[8:15], v[190:197], v[120:123], v170, v171 op_sel_hi:[0,0,0]
	s_waitcnt lgkmcnt(0)
	v_mfma_scale_f32_16x16x128_f8f6f4 v[108:111], v[0:7], v[198:205], v[108:111], v170, v171 op_sel_hi:[0,0,0]
	v_mfma_scale_f32_16x16x128_f8f6f4 v[104:107], v[8:15], v[198:205], v[104:107], v170, v171 op_sel_hi:[0,0,0]
	s_setprio 0
	s_setprio 1
	v_mfma_scale_f32_16x16x128_f8f6f4 v[148:151], v[16:23], v[174:181], v[148:151], v170, v171 op_sel_hi:[0,0,0]
	v_mfma_scale_f32_16x16x128_f8f6f4 v[144:147], v[24:31], v[174:181], v[144:147], v170, v171 op_sel_hi:[0,0,0]
	v_mfma_scale_f32_16x16x128_f8f6f4 v[132:135], v[16:23], v[182:189], v[132:135], v170, v171 op_sel_hi:[0,0,0]
	v_mfma_scale_f32_16x16x128_f8f6f4 v[128:131], v[24:31], v[182:189], v[128:131], v170, v171 op_sel_hi:[0,0,0]
	v_mfma_scale_f32_16x16x128_f8f6f4 v[116:119], v[16:23], v[190:197], v[116:119], v170, v171 op_sel_hi:[0,0,0]
	v_mfma_scale_f32_16x16x128_f8f6f4 v[112:115], v[24:31], v[190:197], v[112:115], v170, v171 op_sel_hi:[0,0,0]
	v_mfma_scale_f32_16x16x128_f8f6f4 v[100:103], v[16:23], v[198:205], v[100:103], v170, v171 op_sel_hi:[0,0,0]
	v_mfma_scale_f32_16x16x128_f8f6f4 v[96:99], v[24:31], v[198:205], v[96:99], v170, v171 op_sel_hi:[0,0,0]
	s_setprio 0
	s_barrier
	ds_read_b128 v[174:177], v169 offset:49152
	ds_read_b128 v[178:181], v169 offset:50176
	ds_read_b128 v[182:185], v169 offset:51200
	ds_read_b128 v[186:189], v169 offset:52224
	ds_read_b128 v[190:193], v169 offset:53248
	ds_read_b128 v[194:197], v169 offset:54272
	ds_read_b128 v[198:201], v169 offset:55296
	ds_read_b128 v[202:205], v169 offset:56320
	s_add_u32 s22, s52, 0x80
	s_addc_u32 s23, s53, 0
	s_mov_b32 m0, s69
	s_nop 0
	global_load_lds_dwordx4 v162, s[22:23]
	s_nop 0
	s_mov_b32 m0, s70
	s_nop 0
	global_load_lds_dwordx4 v167, s[22:23]
	s_add_u32 s22, s52, 0x40080
	s_addc_u32 s23, s53, 0
	s_waitcnt vmcnt(4)
	s_waitcnt lgkmcnt(0)
	s_barrier
	s_setprio 1
	s_waitcnt lgkmcnt(6)
	v_mfma_scale_f32_16x16x128_f8f6f4 v[92:95], v[0:7], v[174:181], v[92:95], v170, v171 op_sel_hi:[0,0,0]
	v_mfma_scale_f32_16x16x128_f8f6f4 v[88:91], v[8:15], v[174:181], v[88:91], v170, v171 op_sel_hi:[0,0,0]
	s_mov_b32 m0, s73
	s_nop 0
	global_load_lds_dwordx4 v162, s[22:23]
	s_waitcnt lgkmcnt(4)
	v_mfma_scale_f32_16x16x128_f8f6f4 v[76:79], v[0:7], v[182:189], v[76:79], v170, v171 op_sel_hi:[0,0,0]
	v_mfma_scale_f32_16x16x128_f8f6f4 v[72:75], v[8:15], v[182:189], v[72:75], v170, v171 op_sel_hi:[0,0,0]
	s_mov_b32 m0, s74
	s_nop 0
	global_load_lds_dwordx4 v167, s[22:23]
	s_waitcnt lgkmcnt(2)
	v_mfma_scale_f32_16x16x128_f8f6f4 v[52:55], v[0:7], v[190:197], v[52:55], v170, v171 op_sel_hi:[0,0,0]
	v_mfma_scale_f32_16x16x128_f8f6f4 v[48:51], v[8:15], v[190:197], v[48:51], v170, v171 op_sel_hi:[0,0,0]
	s_mov_b32 m0, s71
	s_nop 0
	global_load_lds_dwordx4 v160, s[54:55]
	s_waitcnt lgkmcnt(0)
	v_mfma_scale_f32_16x16x128_f8f6f4 v[36:39], v[0:7], v[198:205], v[36:39], v170, v171 op_sel_hi:[0,0,0]
	v_mfma_scale_f32_16x16x128_f8f6f4 v[32:35], v[8:15], v[198:205], v[32:35], v170, v171 op_sel_hi:[0,0,0]
	s_mov_b32 m0, s72
	s_nop 0
	global_load_lds_dwordx4 v163, s[54:55]
	s_setprio 0
	s_setprio 1
	v_mfma_scale_f32_16x16x128_f8f6f4 v[84:87], v[16:23], v[174:181], v[84:87], v170, v171 op_sel_hi:[0,0,0]
	v_mfma_scale_f32_16x16x128_f8f6f4 v[80:83], v[24:31], v[174:181], v[80:83], v170, v171 op_sel_hi:[0,0,0]
	v_mfma_scale_f32_16x16x128_f8f6f4 v[68:71], v[16:23], v[182:189], v[68:71], v170, v171 op_sel_hi:[0,0,0]
	v_mfma_scale_f32_16x16x128_f8f6f4 v[56:59], v[24:31], v[182:189], v[56:59], v170, v171 op_sel_hi:[0,0,0]
	v_mfma_scale_f32_16x16x128_f8f6f4 v[64:67], v[16:23], v[190:197], v[64:67], v170, v171 op_sel_hi:[0,0,0]
	v_mfma_scale_f32_16x16x128_f8f6f4 v[60:63], v[24:31], v[190:197], v[60:63], v170, v171 op_sel_hi:[0,0,0]
	v_mfma_scale_f32_16x16x128_f8f6f4 v[44:47], v[16:23], v[198:205], v[44:47], v170, v171 op_sel_hi:[0,0,0]
	v_mfma_scale_f32_16x16x128_f8f6f4 v[40:43], v[24:31], v[198:205], v[40:43], v170, v171 op_sel_hi:[0,0,0]
	s_setprio 0
	s_barrier
	s_add_i32 s90, s90, 2
	s_add_u32 s88, s88, 0x100
	s_addc_u32 s89, s89, 0
	s_cmp_gt_u32 s90, 13
	s_mov_b64 s[50:51], s[48:49]
	s_cbranch_scc0 .LBB0_2753
	s_and_b64 vcc, exec, s[10:11]
	s_cbranch_vccz .LBB0_2756
	s_barrier
